# attention-A K/V tile images: 8-byte fragment tails of rows 16-31 moved to the upper chunk half (P2 writers, P3 readers) so ds_read_b64 is bank-conflict free
# speedup vs baseline: 1.0765x; 1.0010x over previous
.LBB0_306:
	s_waitcnt lgkmcnt(0)
	global_load_dwordx4 v[0:3], v42, s[10:11] offset:16
	global_load_dwordx4 v[4:7], v42, s[10:11]
	v_add_u32_e32 v32, s26, v13
	s_lshr_b32 s98, s20, 26
	s_lshr_b32 s99, s26, 4
	s_and_b32 s98, s98, s99
	s_bfe_i32 s98, s98, 0x10000
	v_mbcnt_lo_u32_b32 v201, -1, 0
	v_mbcnt_hi_u32_b32 v201, -1, v201
	v_and_b32_e32 v201, 2, v201
	v_lshlrev_b32_e32 v201, 2, v201
	v_and_b32_e32 v202, s98, v201
	v_mov_b32_e32 v203, 0
	v_cvt_f32_fp8_e32 v49, v8
	v_cvt_f32_fp8_sdwa v62, v8 src0_sel:BYTE_1
	v_cvt_f32_fp8_sdwa v63, v8 src0_sel:BYTE_2
	v_cvt_f32_fp8_sdwa v64, v8 src0_sel:BYTE_3
	v_cvt_f32_fp8_e32 v65, v9
	v_cvt_f32_fp8_sdwa v66, v9 src0_sel:BYTE_1
	v_cvt_f32_fp8_sdwa v67, v9 src0_sel:BYTE_2
	v_cvt_f32_fp8_sdwa v68, v9 src0_sel:BYTE_3
	v_and_b32_e32 v8, 63, v32
	v_bfe_u32 v9, v32, 6, 8
	v_and_b32_e32 v11, 64, v41
	v_cndmask_b32_e64 v8, v8, v9, s[4:5]
	v_xor_b32_e32 v10, 1, v41
	v_add_u32_e32 v33, 64, v11
	v_lshlrev_b32_e32 v8, 7, v8
	v_mov_b32_e32 v9, v15
	v_cmp_lt_i32_e32 vcc, v10, v33
	v_lshl_add_u64 v[30:31], v[20:21], 0, v[8:9]
	v_lshl_add_u64 v[46:47], v[30:31], 0, v[14:15]
	v_cndmask_b32_e32 v10, v41, v10, vcc
	v_lshlrev_b32_e32 v45, 2, v10
	global_load_dwordx4 v[8:11], v[46:47], off offset:16
	global_load_dwordx4 v[50:53], v[46:47], off
	global_load_dwordx4 v[54:57], v[30:31], off offset:16
	global_load_dwordx4 v[58:61], v[30:31], off
	v_mul_f32_e32 v69, v62, v62
	v_fmac_f32_e32 v69, v49, v49
	v_fmac_f32_e32 v69, v63, v63
	v_fmac_f32_e32 v69, v64, v64
	v_fmac_f32_e32 v69, v65, v65
	v_fmac_f32_e32 v69, v66, v66
	v_fmac_f32_e32 v69, v67, v67
	v_fmac_f32_e32 v69, v68, v68
	ds_bpermute_b32 v70, v45, v69
	v_xor_b32_e32 v48, 2, v41
	v_cmp_lt_i32_e32 vcc, v48, v33
	v_xor_b32_e32 v46, 4, v41
	s_nop 0
	v_cndmask_b32_e32 v30, v41, v48, vcc
	v_lshlrev_b32_e32 v47, 2, v30
	s_waitcnt lgkmcnt(0)
	v_add_f32_e32 v30, v69, v70
	ds_bpermute_b32 v31, v47, v30
	v_cmp_lt_i32_e32 vcc, v46, v33
	v_xor_b32_e32 v48, 8, v41
	s_waitcnt lgkmcnt(0)
	v_add_f32_e32 v30, v30, v31
	v_cndmask_b32_e32 v46, v41, v46, vcc
	v_lshlrev_b32_e32 v46, 2, v46
	ds_bpermute_b32 v31, v46, v30
	v_cmp_lt_i32_e32 vcc, v48, v33
	s_waitcnt lgkmcnt(0)
	v_add_f32_e32 v30, v30, v31
	v_cndmask_b32_e32 v33, v41, v48, vcc
	v_lshlrev_b32_e32 v48, 2, v33
	ds_bpermute_b32 v31, v48, v30
	s_waitcnt lgkmcnt(0)
	v_add_f32_e32 v30, v30, v31
	v_fmamk_f32 v30, v30, 0x3c000000, v38
	v_mul_f32_e32 v31, 0x4f800000, v30
	v_cmp_gt_f32_e32 vcc, s1, v30
	s_nop 1
	v_cndmask_b32_e32 v30, v30, v31, vcc
	v_sqrt_f32_e32 v31, v30
	s_nop 0
	v_add_u32_e32 v33, -1, v31
	v_fma_f32 v69, -v33, v31, v30
	v_cmp_ge_f32_e64 s[10:11], 0, v69
	v_add_u32_e32 v69, 1, v31
	s_nop 0
	v_cndmask_b32_e64 v33, v31, v33, s[10:11]
	v_fma_f32 v31, -v69, v31, v30
	v_cmp_lt_f32_e64 s[10:11], 0, v31
	s_nop 1
	v_cndmask_b32_e64 v31, v33, v69, s[10:11]
	v_mul_f32_e32 v33, 0x37800000, v31
	v_cndmask_b32_e32 v31, v31, v33, vcc
	v_cmp_class_f32_e32 vcc, v30, v39
	s_nop 1
	v_cndmask_b32_e32 v33, v31, v30, vcc
	v_div_scale_f32 v69, s[10:11], v33, v33, 1.0
	v_rcp_f32_e32 v70, v69
	v_lshl_add_u64 v[30:31], v[22:23], 0, s[20:21]
	v_fma_f32 v71, -v69, v70, 1.0
	v_fmac_f32_e32 v70, v71, v70
	v_div_scale_f32 v71, vcc, 1.0, v33, 1.0
	v_mul_f32_e32 v72, v71, v70
	v_fma_f32 v73, -v69, v72, v71
	v_fmac_f32_e32 v72, v73, v70
	v_fma_f32 v69, -v69, v72, v71
	v_div_fmas_f32 v69, v69, v70, v72
	v_div_fixup_f32 v33, v69, v33, 1.0
	v_mul_f32_e32 v49, v49, v33
	s_waitcnt vmcnt(4)
	v_mul_f32_e32 v49, v4, v49
	ds_bpermute_b32 v69, v46, v49
	v_mul_f32_e32 v63, v63, v33
	v_mul_f32_e32 v63, v6, v63
	v_mul_f32_e32 v65, v65, v33
	v_mul_f32_e32 v65, v0, v65
	s_waitcnt vmcnt(2) lgkmcnt(0)
	v_mul_f32_e32 v50, v50, v69
	v_cndmask_b32_e64 v50, v50, -v50, s[6:7]
	s_waitcnt vmcnt(0)
	v_fmac_f32_e32 v50, v58, v49
	ds_bpermute_b32 v49, v46, v63
	v_mul_f32_e32 v64, v64, v33
	v_mul_f32_e32 v64, v7, v64
	ds_bpermute_b32 v58, v46, v64
	v_mul_f32_e32 v62, v62, v33
	s_waitcnt lgkmcnt(1)
	v_mul_f32_e32 v49, v52, v49
	ds_bpermute_b32 v52, v46, v65
	v_mul_f32_e32 v62, v5, v62
	v_mul_f32_e32 v67, v67, v33
	v_mul_f32_e32 v66, v66, v33
	v_mul_f32_e32 v67, v2, v67
	v_mul_f32_e32 v33, v68, v33
	ds_bpermute_b32 v68, v46, v62
	v_mul_f32_e32 v66, v1, v66
	s_waitcnt lgkmcnt(1)
	v_mul_f32_e32 v8, v8, v52
	ds_bpermute_b32 v52, v46, v67
	v_mul_f32_e32 v53, v53, v58
	ds_bpermute_b32 v58, v46, v66
	v_mul_f32_e32 v33, v3, v33
	s_waitcnt lgkmcnt(2)
	v_mul_f32_e32 v51, v51, v68
	v_cndmask_b32_e64 v51, v51, -v51, s[6:7]
	s_waitcnt lgkmcnt(1)
	v_mul_f32_e32 v10, v10, v52
	ds_bpermute_b32 v52, v46, v33
	v_fmac_f32_e32 v51, v59, v62
	s_waitcnt lgkmcnt(1)
	v_mul_f32_e32 v9, v9, v58
	v_cndmask_b32_e64 v8, v8, -v8, s[6:7]
	v_cndmask_b32_e64 v9, v9, -v9, s[6:7]
	v_mul_f32_e32 v50, s25, v50
	v_mul_f32_e32 v51, s25, v51
	v_fmac_f32_e32 v8, v54, v65
	v_fmac_f32_e32 v9, v55, v66
	v_med3_f32 v50, v50, s2, v40
	v_med3_f32 v51, v51, s2, v40
	v_mov_b32_e32 v54, v15
	v_cndmask_b32_e64 v49, v49, -v49, s[6:7]
	v_cndmask_b32_e64 v53, v53, -v53, s[6:7]
	v_cvt_pk_fp8_f32 v54, v50, v51
	v_mul_f32_e32 v8, s25, v8
	v_mul_f32_e32 v9, s25, v9
	v_fmac_f32_e32 v49, v60, v63
	v_fmac_f32_e32 v53, v61, v64
	s_waitcnt lgkmcnt(0)
	v_mul_f32_e32 v11, v11, v52
	v_med3_f32 v8, v8, s2, v40
	v_med3_f32 v9, v9, s2, v40
	v_mov_b32_e32 v51, v15
	v_cndmask_b32_e64 v10, v10, -v10, s[6:7]
	v_mul_f32_e32 v49, s25, v49
	v_mul_f32_e32 v50, s25, v53
	v_cndmask_b32_e64 v11, v11, -v11, s[6:7]
	v_cvt_pk_fp8_f32 v51, v8, v9
	v_fmac_f32_e32 v10, v56, v67
	v_med3_f32 v49, v49, s2, v40
	v_med3_f32 v50, v50, s2, v40
	v_fmac_f32_e32 v11, v57, v33
	v_cvt_pk_fp8_f32 v54, v49, v50 op_sel:[0,0,1]
	v_mul_f32_e32 v8, s25, v10
	v_mul_f32_e32 v9, s25, v11
	v_med3_f32 v8, v8, s2, v40
	v_med3_f32 v9, v9, s2, v40
	v_cvt_pk_fp8_f32 v51, v8, v9 op_sel:[0,0,1]
	v_lshrrev_b32_e32 v49, 2, v54
	v_and_b32_e32 v33, 0x1f1f1f1f, v54
	v_and_b32_e32 v49, 0x20202020, v49
	v_or_b32_e32 v50, v49, v33
	v_and_b32_e32 v9, 0x1f1f1f1f, v51
	v_lshrrev_b32_e32 v10, 2, v51
	v_bitop3_b32 v33, v49, 63, v33 bitop3:0xc8
	v_lshrrev_b32_e32 v49, 2, v50
	v_and_or_b32 v9, v10, s3, v9
	v_and_or_b32 v33, v49, s13, v33
	v_lshrrev_b32_e32 v49, 4, v50
	v_lshrrev_b32_e32 v8, 6, v50
	v_lshrrev_b32_e32 v10, 2, v9
	v_and_b32_e32 v49, 0x3f000, v49
	v_and_b32_e32 v8, 0xfc0000, v8
	v_and_b32_e32 v10, 0xfc0, v10
	v_or3_b32 v8, v33, v49, v8
	v_or_b32_e32 v11, v10, v9
	v_lshrrev_b32_e32 v33, 4, v9
	v_lshrrev_b32_e32 v9, 6, v9
	v_and_b32_e32 v33, 0x3f000, v33
	v_and_b32_e32 v9, 0xfc0000, v9
	v_or3_b32 v9, v33, v9, v10
	v_lshl_or_b32 v8, v11, 24, v8
	v_lshrrev_b32_e32 v9, 8, v9
	v_mov_b32_e32 v10, v15
	v_mov_b32_e32 v11, v15
	s_nop 0
	v_mov_b32_dpp v10, v8 quad_perm:[1,0,3,2] row_mask:0xf bank_mask:0xf
	v_mov_b32_dpp v11, v9 quad_perm:[1,0,3,2] row_mask:0xf bank_mask:0xf
	s_and_saveexec_b64 s[10:11], s[8:9]
	s_cbranch_execz .LBB0_308
	v_ashrrev_i32_e32 v33, 31, v32
	v_lshlrev_b64 v[50:51], 7, v[32:33]
	v_lshl_add_u64 v[50:51], v[30:31], 0, v[50:51]
	v_lshl_or_b32 v9, v10, 16, v9
	v_perm_b32 v10, v10, v11, s15
	global_store_dword v[50:51], v8, off
	v_lshl_add_u64 v[204:205], v[50:51], 0, v[202:203]
	global_store_dword v[204:205], v9, off offset:4
	global_store_dword v[204:205], v10, off offset:8
.LBB0_308:
	s_or_b64 exec, exec, s[10:11]
	v_cvt_f32_fp8_sdwa v33, v36 src0_sel:BYTE_1
	v_cvt_f32_fp8_e32 v11, v36
	v_cvt_f32_fp8_sdwa v49, v36 src0_sel:BYTE_2
	v_cvt_f32_fp8_sdwa v66, v36 src0_sel:BYTE_3
	v_cvt_f32_fp8_e32 v67, v37
	v_mul_f32_e32 v58, v33, v33
	v_cvt_f32_fp8_sdwa v68, v37 src0_sel:BYTE_1
	v_fmac_f32_e32 v58, v11, v11
	v_cvt_f32_fp8_sdwa v69, v37 src0_sel:BYTE_2
	v_fmac_f32_e32 v58, v49, v49
	v_add_u32_e32 v10, 4, v32
	v_cvt_f32_fp8_sdwa v70, v37 src0_sel:BYTE_3
	v_fmac_f32_e32 v58, v66, v66
	v_and_b32_e32 v8, 63, v10
	v_bfe_u32 v9, v10, 6, 8
	v_fmac_f32_e32 v58, v67, v67
	v_cndmask_b32_e64 v8, v8, v9, s[4:5]
	v_fmac_f32_e32 v58, v68, v68
	v_lshlrev_b32_e32 v8, 7, v8
	v_mov_b32_e32 v9, v15
	v_fmac_f32_e32 v58, v69, v69
	v_lshl_add_u64 v[8:9], v[20:21], 0, v[8:9]
	v_fmac_f32_e32 v58, v70, v70
	v_lshl_add_u64 v[36:37], v[8:9], 0, v[14:15]
	global_load_dwordx4 v[50:53], v[36:37], off
	global_load_dwordx4 v[54:57], v[8:9], off
	ds_bpermute_b32 v59, v45, v58
	s_waitcnt lgkmcnt(0)
	v_add_f32_e32 v58, v58, v59
	ds_bpermute_b32 v59, v47, v58
	s_waitcnt lgkmcnt(0)
	v_add_f32_e32 v71, v58, v59
	global_load_dwordx4 v[58:61], v[36:37], off offset:16
	global_load_dwordx4 v[62:65], v[8:9], off offset:16
	ds_bpermute_b32 v72, v46, v71
	s_waitcnt lgkmcnt(0)
	v_add_f32_e32 v8, v71, v72
	ds_bpermute_b32 v9, v48, v8
	s_waitcnt lgkmcnt(0)
	v_add_f32_e32 v8, v8, v9
	v_fmamk_f32 v8, v8, 0x3c000000, v38
	v_mul_f32_e32 v9, 0x4f800000, v8
	v_cmp_gt_f32_e32 vcc, s1, v8
	s_nop 1
	v_cndmask_b32_e32 v8, v8, v9, vcc
	v_sqrt_f32_e32 v9, v8
	s_nop 0
	v_add_u32_e32 v36, -1, v9
	v_fma_f32 v71, -v36, v9, v8
	v_add_u32_e32 v37, 1, v9
	v_cmp_ge_f32_e64 s[10:11], 0, v71
	s_nop 1
	v_cndmask_b32_e64 v36, v9, v36, s[10:11]
	v_fma_f32 v9, -v37, v9, v8
	v_cmp_lt_f32_e64 s[10:11], 0, v9
	s_nop 1
	v_cndmask_b32_e64 v9, v36, v37, s[10:11]
	v_mul_f32_e32 v36, 0x37800000, v9
	v_cndmask_b32_e32 v9, v9, v36, vcc
	v_cmp_class_f32_e32 vcc, v8, v39
	s_nop 1
	v_cndmask_b32_e32 v8, v9, v8, vcc
	v_div_scale_f32 v9, s[10:11], v8, v8, 1.0
	v_rcp_f32_e32 v36, v9
	v_div_scale_f32 v37, vcc, 1.0, v8, 1.0
	v_fma_f32 v71, -v9, v36, 1.0
	v_fmac_f32_e32 v36, v71, v36
	v_mul_f32_e32 v71, v37, v36
	v_fma_f32 v72, -v9, v71, v37
	v_fmac_f32_e32 v71, v72, v36
	v_fma_f32 v9, -v9, v71, v37
	v_div_fmas_f32 v9, v9, v36, v71
	v_div_fixup_f32 v8, v9, v8, 1.0
	v_mul_f32_e32 v9, v11, v8
	v_mul_f32_e32 v9, v4, v9
	v_mul_f32_e32 v11, v67, v8
	v_mul_f32_e32 v33, v33, v8
	ds_bpermute_b32 v67, v46, v9
	v_mul_f32_e32 v37, v49, v8
	v_mul_f32_e32 v33, v5, v33
	v_mul_f32_e32 v36, v68, v8
	v_mul_f32_e32 v37, v6, v37
	ds_bpermute_b32 v68, v46, v33
	v_mul_f32_e32 v49, v69, v8
	ds_bpermute_b32 v69, v46, v37
	s_waitcnt vmcnt(3) lgkmcnt(2)
	v_mul_f32_e32 v50, v50, v67
	v_cndmask_b32_e64 v50, v50, -v50, s[6:7]
	v_mul_f32_e32 v66, v66, v8
	s_waitcnt vmcnt(2)
	v_fmac_f32_e32 v50, v54, v9
	s_waitcnt lgkmcnt(1)
	v_mul_f32_e32 v9, v51, v68
	v_mul_f32_e32 v66, v7, v66
	v_cndmask_b32_e64 v9, v9, -v9, s[6:7]
	s_waitcnt lgkmcnt(0)
	v_mul_f32_e32 v51, v52, v69
	v_mul_f32_e32 v11, v0, v11
	v_fmac_f32_e32 v9, v55, v33
	ds_bpermute_b32 v33, v46, v66
	v_cndmask_b32_e64 v51, v51, -v51, s[6:7]
	v_fmac_f32_e32 v51, v56, v37
	ds_bpermute_b32 v37, v46, v11
	v_mul_f32_e32 v36, v1, v36
	ds_bpermute_b32 v52, v46, v36
	v_mul_f32_e32 v49, v2, v49
	s_waitcnt lgkmcnt(2)
	v_mul_f32_e32 v33, v53, v33
	ds_bpermute_b32 v53, v46, v49
	s_waitcnt vmcnt(1) lgkmcnt(2)
	v_mul_f32_e32 v37, v58, v37
	v_cndmask_b32_e64 v37, v37, -v37, s[6:7]
	s_waitcnt vmcnt(0)
	v_fmac_f32_e32 v37, v62, v11
	s_waitcnt lgkmcnt(1)
	v_mul_f32_e32 v11, v59, v52
	v_cndmask_b32_e64 v11, v11, -v11, s[6:7]
	v_mul_f32_e32 v8, v70, v8
	v_fmac_f32_e32 v11, v63, v36
	s_waitcnt lgkmcnt(0)
	v_mul_f32_e32 v36, v60, v53
	v_mul_f32_e32 v50, s25, v50
	v_mul_f32_e32 v9, s25, v9
	v_mul_f32_e32 v8, v3, v8
	v_cndmask_b32_e64 v36, v36, -v36, s[6:7]
	v_med3_f32 v50, v50, s2, v40
	v_med3_f32 v9, v9, s2, v40
	v_mov_b32_e32 v52, v15
	v_cndmask_b32_e64 v33, v33, -v33, s[6:7]
	v_fmac_f32_e32 v36, v64, v49
	ds_bpermute_b32 v49, v46, v8
	v_cvt_pk_fp8_f32 v52, v50, v9
	v_fmac_f32_e32 v33, v57, v66
	v_mul_f32_e32 v9, s25, v51
	v_mul_f32_e32 v33, s25, v33
	v_med3_f32 v9, v9, s2, v40
	v_med3_f32 v33, v33, s2, v40
	v_cvt_pk_fp8_f32 v52, v9, v33 op_sel:[0,0,1]
	v_mul_f32_e32 v37, s25, v37
	v_mul_f32_e32 v11, s25, v11
	s_waitcnt lgkmcnt(0)
	v_mul_f32_e32 v9, v61, v49
	v_med3_f32 v37, v37, s2, v40
	v_med3_f32 v11, v11, s2, v40
	v_mov_b32_e32 v50, v15
	v_cndmask_b32_e64 v9, v9, -v9, s[6:7]
	v_cvt_pk_fp8_f32 v50, v37, v11
	v_fmac_f32_e32 v9, v65, v8
	v_lshrrev_b32_e32 v33, 2, v52
	v_mul_f32_e32 v11, s25, v36
	v_mul_f32_e32 v9, s25, v9
	v_and_b32_e32 v8, 0x1f1f1f1f, v52
	v_and_b32_e32 v33, 0x20202020, v33
	v_med3_f32 v11, v11, s2, v40
	v_med3_f32 v9, v9, s2, v40
	v_or_b32_e32 v49, v33, v8
	v_cvt_pk_fp8_f32 v50, v11, v9 op_sel:[0,0,1]
	v_bitop3_b32 v8, v33, 63, v8 bitop3:0xc8
	v_lshrrev_b32_e32 v33, 2, v49
	v_and_or_b32 v8, v33, s13, v8
	v_lshrrev_b32_e32 v33, 4, v49
	v_lshrrev_b32_e32 v9, 6, v49
	v_and_b32_e32 v33, 0x3f000, v33
	v_and_b32_e32 v9, 0xfc0000, v9
	v_or3_b32 v8, v8, v33, v9
	v_and_b32_e32 v9, 0x1f1f1f1f, v50
	v_lshrrev_b32_e32 v11, 2, v50
	v_and_or_b32 v9, v11, s3, v9
	v_lshrrev_b32_e32 v11, 2, v9
	v_and_b32_e32 v11, 0xfc0, v11
	v_or_b32_e32 v33, v11, v9
	v_lshrrev_b32_e32 v36, 4, v9
	v_lshrrev_b32_e32 v9, 6, v9
	v_and_b32_e32 v36, 0x3f000, v36
	v_and_b32_e32 v9, 0xfc0000, v9
	v_or3_b32 v9, v36, v9, v11
	v_lshl_or_b32 v8, v33, 24, v8
	v_lshrrev_b32_e32 v9, 8, v9
	v_mov_b32_e32 v33, v15
	v_mov_b32_e32 v36, v15
	s_nop 0
	v_mov_b32_dpp v33, v8 quad_perm:[1,0,3,2] row_mask:0xf bank_mask:0xf
	v_mov_b32_dpp v36, v9 quad_perm:[1,0,3,2] row_mask:0xf bank_mask:0xf
	s_and_saveexec_b64 s[10:11], s[8:9]
	s_cbranch_execz .LBB0_310
	v_ashrrev_i32_e32 v11, 31, v10
	v_lshlrev_b64 v[10:11], 7, v[10:11]
	v_lshl_add_u64 v[50:51], v[30:31], 0, v[10:11]
	v_lshl_or_b32 v9, v33, 16, v9
	v_perm_b32 v10, v33, v36, s15
	global_store_dword v[50:51], v8, off
	v_lshl_add_u64 v[204:205], v[50:51], 0, v[202:203]
	global_store_dword v[204:205], v9, off offset:4
	global_store_dword v[204:205], v10, off offset:8
.LBB0_310:
	s_or_b64 exec, exec, s[10:11]
	v_cvt_f32_fp8_sdwa v33, v34 src0_sel:BYTE_1
	v_cvt_f32_fp8_e32 v11, v34
	v_cvt_f32_fp8_sdwa v49, v34 src0_sel:BYTE_2
	v_cvt_f32_fp8_sdwa v64, v34 src0_sel:BYTE_3
	v_cvt_f32_fp8_e32 v65, v35
	v_mul_f32_e32 v54, v33, v33
	v_add_u32_e32 v10, 8, v32
	v_cvt_f32_fp8_sdwa v66, v35 src0_sel:BYTE_1
	v_fmac_f32_e32 v54, v11, v11
	v_and_b32_e32 v8, 63, v10
	v_bfe_u32 v9, v10, 6, 8
	v_cvt_f32_fp8_sdwa v67, v35 src0_sel:BYTE_2
	v_fmac_f32_e32 v54, v49, v49
	v_cndmask_b32_e64 v8, v8, v9, s[4:5]
	v_cvt_f32_fp8_sdwa v68, v35 src0_sel:BYTE_3
	v_fmac_f32_e32 v54, v64, v64
	v_lshlrev_b32_e32 v8, 7, v8
	v_mov_b32_e32 v9, v15
	v_fmac_f32_e32 v54, v65, v65
	v_lshl_add_u64 v[8:9], v[20:21], 0, v[8:9]
	v_fmac_f32_e32 v54, v66, v66
	v_lshl_add_u64 v[62:63], v[8:9], 0, v[14:15]
	v_fmac_f32_e32 v54, v67, v67
	global_load_dwordx4 v[34:37], v[62:63], off
	global_load_dwordx4 v[50:53], v[8:9], off
	v_fmac_f32_e32 v54, v68, v68
	ds_bpermute_b32 v55, v45, v54
	s_waitcnt lgkmcnt(0)
	v_add_f32_e32 v54, v54, v55
	ds_bpermute_b32 v55, v47, v54
	s_waitcnt lgkmcnt(0)
	v_add_f32_e32 v69, v54, v55
	global_load_dwordx4 v[54:57], v[62:63], off offset:16
	global_load_dwordx4 v[58:61], v[8:9], off offset:16
	ds_bpermute_b32 v70, v46, v69
	s_waitcnt lgkmcnt(0)
	v_add_f32_e32 v8, v69, v70
	ds_bpermute_b32 v9, v48, v8
	s_waitcnt lgkmcnt(0)
	v_add_f32_e32 v8, v8, v9
	v_fmamk_f32 v8, v8, 0x3c000000, v38
	v_mul_f32_e32 v9, 0x4f800000, v8
	v_cmp_gt_f32_e32 vcc, s1, v8
	s_nop 1
	v_cndmask_b32_e32 v8, v8, v9, vcc
	v_sqrt_f32_e32 v9, v8
	s_nop 0
	v_add_u32_e32 v62, -1, v9
	v_fma_f32 v69, -v62, v9, v8
	v_add_u32_e32 v63, 1, v9
	v_cmp_ge_f32_e64 s[10:11], 0, v69
	s_nop 1
	v_cndmask_b32_e64 v62, v9, v62, s[10:11]
	v_fma_f32 v9, -v63, v9, v8
	v_cmp_lt_f32_e64 s[10:11], 0, v9
	s_nop 1
	v_cndmask_b32_e64 v9, v62, v63, s[10:11]
	v_mul_f32_e32 v62, 0x37800000, v9
	v_cndmask_b32_e32 v9, v9, v62, vcc
	v_cmp_class_f32_e32 vcc, v8, v39
	s_nop 1
	v_cndmask_b32_e32 v8, v9, v8, vcc
	v_div_scale_f32 v9, s[10:11], v8, v8, 1.0
	v_rcp_f32_e32 v62, v9
	v_div_scale_f32 v63, vcc, 1.0, v8, 1.0
	v_fma_f32 v69, -v9, v62, 1.0
	v_fmac_f32_e32 v62, v69, v62
	v_mul_f32_e32 v69, v63, v62
	v_fma_f32 v70, -v9, v69, v63
	v_fmac_f32_e32 v69, v70, v62
	v_fma_f32 v9, -v9, v69, v63
	v_div_fmas_f32 v9, v9, v62, v69
	v_div_fixup_f32 v8, v9, v8, 1.0
	v_mul_f32_e32 v9, v11, v8
	v_mul_f32_e32 v9, v4, v9
	v_mul_f32_e32 v11, v65, v8
	v_mul_f32_e32 v33, v33, v8
	ds_bpermute_b32 v65, v46, v9
	v_mul_f32_e32 v33, v5, v33
	v_mul_f32_e32 v62, v66, v8
	ds_bpermute_b32 v66, v46, v33
	v_mul_f32_e32 v49, v49, v8
	v_mul_f32_e32 v49, v6, v49
	s_waitcnt vmcnt(3) lgkmcnt(1)
	v_mul_f32_e32 v34, v34, v65
	v_cndmask_b32_e64 v34, v34, -v34, s[6:7]
	v_mul_f32_e32 v63, v67, v8
	v_mul_f32_e32 v64, v64, v8
	ds_bpermute_b32 v67, v46, v49
	s_waitcnt vmcnt(2)
	v_fmac_f32_e32 v34, v50, v9
	s_waitcnt lgkmcnt(1)
	v_mul_f32_e32 v9, v35, v66
	v_mul_f32_e32 v64, v7, v64
	v_cndmask_b32_e64 v9, v9, -v9, s[6:7]
	v_fmac_f32_e32 v9, v51, v33
	ds_bpermute_b32 v33, v46, v64
	v_mul_f32_e32 v11, v0, v11
	s_waitcnt lgkmcnt(1)
	v_mul_f32_e32 v35, v36, v67
	ds_bpermute_b32 v36, v46, v11
	v_mul_f32_e32 v62, v1, v62
	v_mul_f32_e32 v63, v2, v63
	v_cndmask_b32_e64 v35, v35, -v35, s[6:7]
	v_fmac_f32_e32 v35, v52, v49
	s_waitcnt lgkmcnt(1)
	v_mul_f32_e32 v33, v37, v33
	ds_bpermute_b32 v37, v46, v62
	ds_bpermute_b32 v49, v46, v63
	v_mul_f32_e32 v8, v68, v8
	s_waitcnt vmcnt(1) lgkmcnt(2)
	v_mul_f32_e32 v36, v54, v36
	v_mul_f32_e32 v34, s25, v34
	v_mul_f32_e32 v9, s25, v9
	v_mul_f32_e32 v8, v3, v8
	v_cndmask_b32_e64 v36, v36, -v36, s[6:7]
	v_med3_f32 v34, v34, s2, v40
	v_med3_f32 v9, v9, s2, v40
	v_mov_b32_e32 v50, v15
	v_cndmask_b32_e64 v33, v33, -v33, s[6:7]
	s_waitcnt vmcnt(0)
	v_fmac_f32_e32 v36, v58, v11
	s_waitcnt lgkmcnt(1)
	v_mul_f32_e32 v11, v55, v37
	s_waitcnt lgkmcnt(0)
	v_mul_f32_e32 v37, v56, v49
	ds_bpermute_b32 v49, v46, v8
	v_cvt_pk_fp8_f32 v50, v34, v9
	v_fmac_f32_e32 v33, v53, v64
	v_cndmask_b32_e64 v11, v11, -v11, s[6:7]
	v_mul_f32_e32 v9, s25, v35
	v_mul_f32_e32 v33, s25, v33
	v_fmac_f32_e32 v11, v59, v62
	v_med3_f32 v9, v9, s2, v40
	v_med3_f32 v33, v33, s2, v40
	v_cvt_pk_fp8_f32 v50, v9, v33 op_sel:[0,0,1]
	v_mul_f32_e32 v35, s25, v36
	v_mul_f32_e32 v11, s25, v11
	s_waitcnt lgkmcnt(0)
	v_mul_f32_e32 v9, v57, v49
	v_med3_f32 v35, v35, s2, v40
	v_med3_f32 v11, v11, s2, v40
	v_mov_b32_e32 v36, v15
	v_cndmask_b32_e64 v37, v37, -v37, s[6:7]
	v_cndmask_b32_e64 v9, v9, -v9, s[6:7]
	v_cvt_pk_fp8_f32 v36, v35, v11
	v_fmac_f32_e32 v37, v60, v63
	v_fmac_f32_e32 v9, v61, v8
	v_lshrrev_b32_e32 v33, 2, v50
	v_mul_f32_e32 v11, s25, v37
	v_mul_f32_e32 v9, s25, v9
	v_and_b32_e32 v8, 0x1f1f1f1f, v50
	v_and_b32_e32 v33, 0x20202020, v33
	v_med3_f32 v11, v11, s2, v40
	v_med3_f32 v9, v9, s2, v40
	v_or_b32_e32 v34, v33, v8
	v_cvt_pk_fp8_f32 v36, v11, v9 op_sel:[0,0,1]
	v_bitop3_b32 v8, v33, 63, v8 bitop3:0xc8
	v_lshrrev_b32_e32 v33, 2, v34
	v_and_or_b32 v8, v33, s13, v8
	v_lshrrev_b32_e32 v33, 4, v34
	v_lshrrev_b32_e32 v9, 6, v34
	v_and_b32_e32 v33, 0x3f000, v33
	v_and_b32_e32 v9, 0xfc0000, v9
	v_or3_b32 v8, v8, v33, v9
	v_and_b32_e32 v9, 0x1f1f1f1f, v36
	v_lshrrev_b32_e32 v11, 2, v36
	v_and_or_b32 v9, v11, s3, v9
	v_lshrrev_b32_e32 v11, 2, v9
	v_and_b32_e32 v11, 0xfc0, v11
	v_or_b32_e32 v33, v11, v9
	v_lshrrev_b32_e32 v34, 4, v9
	v_lshrrev_b32_e32 v9, 6, v9
	v_and_b32_e32 v34, 0x3f000, v34
	v_and_b32_e32 v9, 0xfc0000, v9
	v_or3_b32 v9, v34, v9, v11
	v_lshl_or_b32 v8, v33, 24, v8
	v_lshrrev_b32_e32 v9, 8, v9
	v_mov_b32_e32 v33, v15
	v_mov_b32_e32 v34, v15
	s_nop 0
	v_mov_b32_dpp v33, v8 quad_perm:[1,0,3,2] row_mask:0xf bank_mask:0xf
	v_mov_b32_dpp v34, v9 quad_perm:[1,0,3,2] row_mask:0xf bank_mask:0xf
	s_and_saveexec_b64 s[10:11], s[8:9]
	s_cbranch_execz .LBB0_312
	v_ashrrev_i32_e32 v11, 31, v10
	v_lshlrev_b64 v[10:11], 7, v[10:11]
	v_lshl_add_u64 v[36:37], v[30:31], 0, v[10:11]
	v_lshl_or_b32 v9, v33, 16, v9
	v_perm_b32 v10, v33, v34, s15
	global_store_dword v[36:37], v8, off
	v_lshl_add_u64 v[204:205], v[36:37], 0, v[202:203]
	global_store_dword v[204:205], v9, off offset:4
	global_store_dword v[204:205], v10, off offset:8
.LBB0_312:
	s_or_b64 exec, exec, s[10:11]
	s_nop 0
	v_add_u32_e32 v8, 12, v32
	v_and_b32_e32 v10, 63, v8
	v_bfe_u32 v11, v8, 6, 8
	v_cndmask_b32_e64 v10, v10, v11, s[4:5]
	v_lshlrev_b32_e32 v10, 7, v10
	v_mov_b32_e32 v11, v15
	v_cvt_f32_fp8_sdwa v49, v44 src0_sel:BYTE_1
	v_lshl_add_u64 v[10:11], v[20:21], 0, v[10:11]
	v_cvt_f32_fp8_e32 v9, v44
	v_lshl_add_u64 v[36:37], v[10:11], 0, v[14:15]
	v_cvt_f32_fp8_sdwa v62, v44 src0_sel:BYTE_2
	global_load_dwordx4 v[32:35], v[36:37], off
	global_load_dwordx4 v[50:53], v[10:11], off
	v_cvt_f32_fp8_sdwa v44, v44 src0_sel:BYTE_3
	v_cvt_f32_fp8_e32 v63, v43
	v_mul_f32_e32 v54, v49, v49
	v_cvt_f32_fp8_sdwa v64, v43 src0_sel:BYTE_1
	v_fmac_f32_e32 v54, v9, v9
	v_cvt_f32_fp8_sdwa v65, v43 src0_sel:BYTE_2
	v_fmac_f32_e32 v54, v62, v62
	v_cvt_f32_fp8_sdwa v43, v43 src0_sel:BYTE_3
	v_fmac_f32_e32 v54, v44, v44
	v_fmac_f32_e32 v54, v63, v63
	v_fmac_f32_e32 v54, v64, v64
	v_fmac_f32_e32 v54, v65, v65
	v_fmac_f32_e32 v54, v43, v43
	ds_bpermute_b32 v45, v45, v54
	s_waitcnt lgkmcnt(0)
	v_add_f32_e32 v45, v54, v45
	global_load_dwordx4 v[54:57], v[36:37], off offset:16
	global_load_dwordx4 v[58:61], v[10:11], off offset:16
	ds_bpermute_b32 v47, v47, v45
	s_waitcnt lgkmcnt(0)
	v_add_f32_e32 v45, v45, v47
	ds_bpermute_b32 v47, v46, v45
	s_waitcnt lgkmcnt(0)
	v_add_f32_e32 v10, v45, v47
	ds_bpermute_b32 v11, v48, v10
	s_waitcnt lgkmcnt(0)
	v_add_f32_e32 v10, v10, v11
	v_fmamk_f32 v10, v10, 0x3c000000, v38
	v_mul_f32_e32 v11, 0x4f800000, v10
	v_cmp_gt_f32_e32 vcc, s1, v10
	s_nop 1
	v_cndmask_b32_e32 v10, v10, v11, vcc
	v_sqrt_f32_e32 v11, v10
	s_nop 0
	v_add_u32_e32 v36, -1, v11
	v_fma_f32 v45, -v36, v11, v10
	v_add_u32_e32 v37, 1, v11
	v_cmp_ge_f32_e64 s[10:11], 0, v45
	s_nop 1
	v_cndmask_b32_e64 v36, v11, v36, s[10:11]
	v_fma_f32 v11, -v37, v11, v10
	v_cmp_lt_f32_e64 s[10:11], 0, v11
	s_nop 1
	v_cndmask_b32_e64 v11, v36, v37, s[10:11]
	v_mul_f32_e32 v36, 0x37800000, v11
	v_cndmask_b32_e32 v11, v11, v36, vcc
	v_cmp_class_f32_e32 vcc, v10, v39
	s_nop 1
	v_cndmask_b32_e32 v10, v11, v10, vcc
	v_div_scale_f32 v11, s[10:11], v10, v10, 1.0
	v_rcp_f32_e32 v36, v11
	v_div_scale_f32 v37, vcc, 1.0, v10, 1.0
	v_fma_f32 v45, -v11, v36, 1.0
	v_fmac_f32_e32 v36, v45, v36
	v_mul_f32_e32 v45, v37, v36
	v_fma_f32 v47, -v11, v45, v37
	v_fmac_f32_e32 v45, v47, v36
	v_fma_f32 v11, -v11, v45, v37
	v_div_fmas_f32 v11, v11, v36, v45
	v_div_fixup_f32 v10, v11, v10, 1.0
	v_mul_f32_e32 v9, v9, v10
	v_mul_f32_e32 v4, v4, v9
	v_mul_f32_e32 v36, v49, v10
	ds_bpermute_b32 v9, v46, v4
	v_mul_f32_e32 v11, v63, v10
	v_mul_f32_e32 v37, v64, v10
	v_mul_f32_e32 v45, v62, v10
	v_mul_f32_e32 v47, v65, v10
	v_mul_f32_e32 v44, v44, v10
	v_mul_f32_e32 v10, v43, v10
	v_mul_f32_e32 v5, v5, v36
	v_mul_f32_e32 v3, v3, v10
	ds_bpermute_b32 v10, v46, v5
	s_waitcnt vmcnt(3) lgkmcnt(1)
	v_mul_f32_e32 v9, v32, v9
	v_mul_f32_e32 v6, v6, v45
	v_cndmask_b32_e64 v9, v9, -v9, s[6:7]
	v_mul_f32_e32 v0, v0, v11
	ds_bpermute_b32 v11, v46, v6
	s_waitcnt vmcnt(2)
	v_fmac_f32_e32 v9, v50, v4
	s_waitcnt lgkmcnt(1)
	v_mul_f32_e32 v4, v33, v10
	v_mul_f32_e32 v7, v7, v44
	v_cndmask_b32_e64 v4, v4, -v4, s[6:7]
	v_fmac_f32_e32 v4, v51, v5
	ds_bpermute_b32 v5, v46, v7
	s_waitcnt lgkmcnt(1)
	v_mul_f32_e32 v10, v34, v11
	v_cndmask_b32_e64 v10, v10, -v10, s[6:7]
	v_fmac_f32_e32 v10, v52, v6
	ds_bpermute_b32 v6, v46, v0
	s_waitcnt lgkmcnt(1)
	v_mul_f32_e32 v5, v35, v5
	v_mul_f32_e32 v1, v1, v37
	v_cndmask_b32_e64 v5, v5, -v5, s[6:7]
	v_fmac_f32_e32 v5, v53, v7
	ds_bpermute_b32 v7, v46, v1
	v_mul_f32_e32 v2, v2, v47
	ds_bpermute_b32 v11, v46, v2
	s_waitcnt vmcnt(1) lgkmcnt(2)
	v_mul_f32_e32 v6, v54, v6
	v_cndmask_b32_e64 v6, v6, -v6, s[6:7]
	s_waitcnt vmcnt(0)
	v_fmac_f32_e32 v6, v58, v0
	s_waitcnt lgkmcnt(1)
	v_mul_f32_e32 v0, v55, v7
	v_cndmask_b32_e64 v0, v0, -v0, s[6:7]
	v_fmac_f32_e32 v0, v59, v1
	s_waitcnt lgkmcnt(0)
	v_mul_f32_e32 v1, v56, v11
	v_cndmask_b32_e64 v1, v1, -v1, s[6:7]
	v_fmac_f32_e32 v1, v60, v2
	ds_bpermute_b32 v2, v46, v3
	v_mul_f32_e32 v7, s25, v9
	v_mul_f32_e32 v4, s25, v4
	v_med3_f32 v7, v7, s2, v40
	v_med3_f32 v4, v4, s2, v40
	v_mov_b32_e32 v9, v15
	v_cvt_pk_fp8_f32 v9, v7, v4
	v_mul_f32_e32 v6, s25, v6
	v_mul_f32_e32 v0, s25, v0
	s_waitcnt lgkmcnt(0)
	v_mul_f32_e32 v2, v57, v2
	v_med3_f32 v6, v6, s2, v40
	v_med3_f32 v0, v0, s2, v40
	v_mov_b32_e32 v7, v15
	v_mul_f32_e32 v4, s25, v10
	v_mul_f32_e32 v5, s25, v5
	v_cndmask_b32_e64 v2, v2, -v2, s[6:7]
	v_cvt_pk_fp8_f32 v7, v6, v0
	v_med3_f32 v4, v4, s2, v40
	v_med3_f32 v5, v5, s2, v40
	v_fmac_f32_e32 v2, v61, v3
	v_cvt_pk_fp8_f32 v9, v4, v5 op_sel:[0,0,1]
	v_mul_f32_e32 v0, s25, v1
	v_mul_f32_e32 v1, s25, v2
	v_med3_f32 v0, v0, s2, v40
	v_med3_f32 v1, v1, s2, v40
	v_cvt_pk_fp8_f32 v7, v0, v1 op_sel:[0,0,1]
	v_lshrrev_b32_e32 v4, 2, v9
	v_and_b32_e32 v3, 0x1f1f1f1f, v9
	v_and_b32_e32 v4, 0x20202020, v4
	v_or_b32_e32 v5, v4, v3
	v_and_b32_e32 v1, 0x1f1f1f1f, v7
	v_lshrrev_b32_e32 v2, 2, v7
	v_bitop3_b32 v3, v4, 63, v3 bitop3:0xc8
	v_lshrrev_b32_e32 v4, 2, v5
	v_and_or_b32 v1, v2, s3, v1
	v_and_or_b32 v3, v4, s13, v3
	v_lshrrev_b32_e32 v4, 4, v5
	v_lshrrev_b32_e32 v0, 6, v5
	v_lshrrev_b32_e32 v2, 2, v1
	v_and_b32_e32 v4, 0x3f000, v4
	v_and_b32_e32 v0, 0xfc0000, v0
	v_and_b32_e32 v2, 0xfc0, v2
	v_or3_b32 v0, v3, v4, v0
	v_or_b32_e32 v3, v2, v1
	v_lshrrev_b32_e32 v4, 4, v1
	v_lshrrev_b32_e32 v1, 6, v1
	v_and_b32_e32 v4, 0x3f000, v4
	v_and_b32_e32 v1, 0xfc0000, v1
	v_or3_b32 v1, v4, v1, v2
	v_lshl_or_b32 v0, v3, 24, v0
	v_lshrrev_b32_e32 v1, 8, v1
	v_mov_b32_e32 v2, v15
	v_mov_b32_e32 v3, v15
	s_nop 0
	v_mov_b32_dpp v2, v0 quad_perm:[1,0,3,2] row_mask:0xf bank_mask:0xf
	v_mov_b32_dpp v3, v1 quad_perm:[1,0,3,2] row_mask:0xf bank_mask:0xf
	s_and_saveexec_b64 s[10:11], s[8:9]
	s_cbranch_execz .LBB0_298
	v_ashrrev_i32_e32 v9, 31, v8
	v_lshlrev_b64 v[4:5], 7, v[8:9]
	v_lshl_add_u64 v[4:5], v[30:31], 0, v[4:5]
	v_lshl_or_b32 v1, v2, 16, v1
	v_perm_b32 v2, v2, v3, s15
	global_store_dword v[4:5], v0, off
	v_lshl_add_u64 v[204:205], v[4:5], 0, v[202:203]
	global_store_dword v[204:205], v1, off offset:4
	global_store_dword v[204:205], v2, off offset:8
	s_branch .LBB0_298

.LBB0_316:
	v_lshl_add_u64 v[8:9], s[6:7], 0, v[2:3]
	v_lshl_add_u64 v[6:7], s[6:7], 0, v[0:1]
	v_add_co_u32_e64 v10, s[4:5], s2, v8
	v_lshl_add_u64 v[48:49], s[6:7], 0, v[4:5]
	v_add_co_u32_e32 v82, vcc, 0x49000000, v6
	v_addc_co_u32_e64 v11, s[4:5], 0, v9, s[4:5]
	v_lshl_add_u64 v[80:81], v[6:7], 0, s[10:11]
	v_add_co_u32_e64 v8, s[4:5], s2, v48
	v_addc_co_u32_e32 v83, vcc, 0, v7, vcc
	v_lshl_add_u64 v[84:85], v[6:7], 0, s[16:17]
	v_addc_co_u32_e64 v9, s[4:5], 0, v49, s[4:5]
	global_load_dwordx4 v[48:51], v[80:81], off offset:16
	global_load_dwordx4 v[52:55], v[80:81], off offset:32
	global_load_dwordx4 v[56:59], v[84:85], off offset:32
	global_load_dwordx4 v[60:63], v[84:85], off offset:48
	global_load_dwordx4 v[64:67], v[82:83], off
	global_load_dwordx4 v[68:71], v[80:81], off offset:48
	global_load_dwordx4 v[72:75], v[82:83], off offset:64
	global_load_dwordx4 v[76:79], v[84:85], off offset:16
	v_mov_b32_e32 v19, 0
	v_mov_b32_e32 v20, 0
	v_mov_b32_e32 v21, 0
	v_mov_b32_e32 v22, 0
	v_mov_b32_e32 v23, 0
	v_mov_b32_e32 v24, 0
	v_mov_b32_e32 v25, 0
	v_mov_b32_e32 v27, 0
	v_mov_b32_e32 v39, 0
	v_mov_b32_e32 v40, 0
	v_mov_b32_e32 v41, 0
	v_mov_b32_e32 v42, 0
	v_mov_b32_e32 v15, 0
	v_mov_b32_e32 v16, 0
	v_mov_b32_e32 v17, 0
	v_mov_b32_e32 v18, 0
	v_mov_b32_e32 v26, 0
	v_mov_b32_e32 v28, 0
	v_mov_b32_e32 v29, 0
	v_mov_b32_e32 v30, 0
	v_mov_b32_e32 v31, 0
	v_mov_b32_e32 v32, 0
	v_mov_b32_e32 v33, 0
	v_mov_b32_e32 v34, 0
	v_mov_b32_e32 v35, 0
	v_mov_b32_e32 v36, 0
	v_mov_b32_e32 v37, 0
	v_mov_b32_e32 v38, 0
	v_mov_b32_e32 v43, 0
	v_mov_b32_e32 v44, 0
	v_mov_b32_e32 v45, 0
	v_mov_b32_e32 v46, 0
	s_add_i32 s12, s12, s14
	s_add_u32 s6, s6, s8
	s_addc_u32 s7, s7, s9
	s_cmpk_lt_i32 s12, 0x400
	s_waitcnt vmcnt(7)
	v_cvt_f32_fp8_e32 v6, v48
	v_cvt_f32_fp8_sdwa v7, v48 src0_sel:BYTE_1
	v_cvt_f32_fp8_e32 v80, v49
	v_cvt_f32_fp8_sdwa v81, v49 src0_sel:BYTE_1
	v_cvt_f32_fp8_e32 v83, v50
	v_cvt_f32_fp8_sdwa v84, v50 src0_sel:BYTE_1
	v_cvt_f32_fp8_e32 v86, v51
	v_cvt_f32_fp8_sdwa v87, v51 src0_sel:BYTE_1
	s_waitcnt vmcnt(6)
	v_cvt_f32_fp8_e32 v89, v52
	v_cvt_f32_fp8_sdwa v90, v52 src0_sel:BYTE_1
	v_cvt_f32_fp8_e32 v92, v53
	v_cvt_f32_fp8_sdwa v93, v53 src0_sel:BYTE_1
	v_cvt_f32_fp8_e32 v95, v54
	v_cvt_f32_fp8_sdwa v96, v54 src0_sel:BYTE_1
	v_cvt_f32_fp8_e32 v98, v55
	v_cvt_f32_fp8_sdwa v99, v55 src0_sel:BYTE_1
	s_waitcnt vmcnt(5)
	v_cvt_f32_fp8_e32 v101, v56
	v_cvt_f32_fp8_sdwa v102, v56 src0_sel:BYTE_1
	v_cvt_f32_fp8_e32 v104, v57
	v_cvt_f32_fp8_sdwa v105, v57 src0_sel:BYTE_1
	v_cvt_f32_fp8_e32 v107, v58
	v_cvt_f32_fp8_sdwa v108, v58 src0_sel:BYTE_1
	v_cvt_f32_fp8_e32 v110, v59
	v_cvt_f32_fp8_sdwa v111, v59 src0_sel:BYTE_1
	s_waitcnt vmcnt(4)
	v_cvt_f32_fp8_e32 v113, v60
	v_cvt_f32_fp8_sdwa v114, v60 src0_sel:BYTE_1
	v_cvt_f32_fp8_e32 v116, v61
	v_cvt_f32_fp8_sdwa v117, v61 src0_sel:BYTE_1
	v_cvt_f32_fp8_e32 v119, v62
	v_cvt_f32_fp8_sdwa v120, v62 src0_sel:BYTE_1
	v_cvt_f32_fp8_e32 v122, v63
	v_cvt_f32_fp8_sdwa v123, v63 src0_sel:BYTE_1
	s_waitcnt vmcnt(3)
	v_cvt_f32_fp8_e32 v125, v64
	v_cvt_f32_fp8_sdwa v126, v64 src0_sel:BYTE_1
	v_cvt_f32_fp8_e32 v128, v65
	v_cvt_f32_fp8_sdwa v129, v65 src0_sel:BYTE_1
	v_cvt_f32_fp8_e32 v131, v66
	v_cvt_f32_fp8_sdwa v132, v66 src0_sel:BYTE_1
	v_cvt_f32_fp8_e32 v134, v67
	v_cvt_f32_fp8_sdwa v135, v67 src0_sel:BYTE_1
	s_waitcnt vmcnt(2)
	v_cvt_f32_fp8_e32 v137, v68
	v_cvt_f32_fp8_sdwa v138, v68 src0_sel:BYTE_1
	v_cvt_f32_fp8_sdwa v139, v68 src0_sel:BYTE_2
	v_cvt_f32_fp8_e32 v140, v69
	v_cvt_f32_fp8_sdwa v141, v69 src0_sel:BYTE_1
	v_cvt_f32_fp8_sdwa v142, v69 src0_sel:BYTE_2
	v_cvt_f32_fp8_e32 v143, v70
	v_cvt_f32_fp8_sdwa v144, v70 src0_sel:BYTE_1
	v_cvt_f32_fp8_sdwa v145, v70 src0_sel:BYTE_2
	v_cvt_f32_fp8_e32 v146, v71
	v_cvt_f32_fp8_sdwa v147, v71 src0_sel:BYTE_1
	v_cvt_f32_fp8_sdwa v148, v71 src0_sel:BYTE_2
	s_waitcnt vmcnt(1)
	v_cvt_f32_fp8_e32 v149, v72
	v_cvt_f32_fp8_sdwa v150, v72 src0_sel:BYTE_1
	v_cvt_f32_fp8_sdwa v151, v72 src0_sel:BYTE_2
	v_cvt_f32_fp8_e32 v152, v73
	v_cvt_f32_fp8_sdwa v153, v73 src0_sel:BYTE_1
	v_cvt_f32_fp8_sdwa v154, v73 src0_sel:BYTE_2
	v_cvt_f32_fp8_e32 v155, v74
	v_cvt_f32_fp8_sdwa v156, v74 src0_sel:BYTE_1
	v_cvt_f32_fp8_e32 v158, v75
	v_cvt_f32_fp8_sdwa v159, v75 src0_sel:BYTE_1
	s_waitcnt vmcnt(0)
	v_cvt_f32_fp8_e32 v161, v76
	v_cvt_f32_fp8_sdwa v162, v76 src0_sel:BYTE_1
	v_cvt_f32_fp8_e32 v164, v77
	v_cvt_f32_fp8_sdwa v165, v77 src0_sel:BYTE_1
	v_cvt_f32_fp8_e32 v167, v78
	v_cvt_f32_fp8_sdwa v168, v78 src0_sel:BYTE_1
	v_cvt_f32_fp8_e32 v170, v79
	v_cvt_f32_fp8_sdwa v171, v79 src0_sel:BYTE_1
	v_cvt_f32_fp8_sdwa v47, v48 src0_sel:BYTE_2
	v_cvt_f32_fp8_sdwa v48, v48 src0_sel:BYTE_3
	v_cvt_f32_fp8_sdwa v82, v49 src0_sel:BYTE_2
	v_cvt_f32_fp8_sdwa v49, v49 src0_sel:BYTE_3
	v_cvt_f32_fp8_sdwa v85, v50 src0_sel:BYTE_2
	v_cvt_f32_fp8_sdwa v50, v50 src0_sel:BYTE_3
	v_cvt_f32_fp8_sdwa v88, v51 src0_sel:BYTE_2
	v_cvt_f32_fp8_sdwa v51, v51 src0_sel:BYTE_3
	v_cvt_f32_fp8_sdwa v91, v52 src0_sel:BYTE_2
	v_cvt_f32_fp8_sdwa v52, v52 src0_sel:BYTE_3
	v_cvt_f32_fp8_sdwa v94, v53 src0_sel:BYTE_2
	v_cvt_f32_fp8_sdwa v53, v53 src0_sel:BYTE_3
	v_cvt_f32_fp8_sdwa v97, v54 src0_sel:BYTE_2
	v_cvt_f32_fp8_sdwa v54, v54 src0_sel:BYTE_3
	v_cvt_f32_fp8_sdwa v100, v55 src0_sel:BYTE_2
	v_cvt_f32_fp8_sdwa v55, v55 src0_sel:BYTE_3
	v_cvt_f32_fp8_sdwa v103, v56 src0_sel:BYTE_2
	v_cvt_f32_fp8_sdwa v56, v56 src0_sel:BYTE_3
	v_cvt_f32_fp8_sdwa v106, v57 src0_sel:BYTE_2
	v_cvt_f32_fp8_sdwa v57, v57 src0_sel:BYTE_3
	v_cvt_f32_fp8_sdwa v109, v58 src0_sel:BYTE_2
	v_cvt_f32_fp8_sdwa v58, v58 src0_sel:BYTE_3
	v_cvt_f32_fp8_sdwa v112, v59 src0_sel:BYTE_2
	v_cvt_f32_fp8_sdwa v59, v59 src0_sel:BYTE_3
	v_mul_f32_e32 v6, 0x3d000000, v6
	v_mul_f32_e32 v7, 0x3d000000, v7
	v_mul_f32_e32 v80, 0x3d000000, v80
	v_mul_f32_e32 v81, 0x3d000000, v81
	v_mul_f32_e32 v83, 0x3d000000, v83
	v_mul_f32_e32 v84, 0x3d000000, v84
	v_mul_f32_e32 v86, 0x3d000000, v86
	v_mul_f32_e32 v87, 0x3d000000, v87
	v_mul_f32_e32 v89, 0x3d000000, v89
	v_mul_f32_e32 v90, 0x3d000000, v90
	v_mul_f32_e32 v92, 0x3d000000, v92
	v_mul_f32_e32 v93, 0x3d000000, v93
	v_mul_f32_e32 v95, 0x3d000000, v95
	v_mul_f32_e32 v96, 0x3d000000, v96
	v_mul_f32_e32 v98, 0x3d000000, v98
	v_mul_f32_e32 v99, 0x3d000000, v99
	v_mul_f32_e32 v101, 0x3d000000, v101
	v_mul_f32_e32 v102, 0x3d000000, v102
	v_mul_f32_e32 v104, 0x3d000000, v104
	v_mul_f32_e32 v105, 0x3d000000, v105
	v_mul_f32_e32 v107, 0x3d000000, v107
	v_mul_f32_e32 v108, 0x3d000000, v108
	v_mul_f32_e32 v110, 0x3d000000, v110
	v_mul_f32_e32 v111, 0x3d000000, v111
	v_cvt_f32_fp8_sdwa v115, v60 src0_sel:BYTE_2
	v_cvt_f32_fp8_sdwa v60, v60 src0_sel:BYTE_3
	v_cvt_f32_fp8_sdwa v118, v61 src0_sel:BYTE_2
	v_cvt_f32_fp8_sdwa v61, v61 src0_sel:BYTE_3
	v_cvt_f32_fp8_sdwa v121, v62 src0_sel:BYTE_2
	v_cvt_f32_fp8_sdwa v62, v62 src0_sel:BYTE_3
	v_cvt_f32_fp8_sdwa v124, v63 src0_sel:BYTE_2
	v_cvt_f32_fp8_sdwa v63, v63 src0_sel:BYTE_3
	v_cvt_f32_fp8_sdwa v127, v64 src0_sel:BYTE_2
	v_cvt_f32_fp8_sdwa v64, v64 src0_sel:BYTE_3
	v_cvt_f32_fp8_sdwa v130, v65 src0_sel:BYTE_2
	v_cvt_f32_fp8_sdwa v65, v65 src0_sel:BYTE_3
	v_cvt_f32_fp8_sdwa v133, v66 src0_sel:BYTE_2
	v_cvt_f32_fp8_sdwa v66, v66 src0_sel:BYTE_3
	v_cvt_f32_fp8_sdwa v136, v67 src0_sel:BYTE_2
	v_cvt_f32_fp8_sdwa v67, v67 src0_sel:BYTE_3
	v_cvt_f32_fp8_sdwa v68, v68 src0_sel:BYTE_3
	v_cvt_f32_fp8_sdwa v69, v69 src0_sel:BYTE_3
	v_cvt_f32_fp8_sdwa v70, v70 src0_sel:BYTE_3
	v_cvt_f32_fp8_sdwa v71, v71 src0_sel:BYTE_3
	v_cvt_f32_fp8_sdwa v72, v72 src0_sel:BYTE_3
	v_cvt_f32_fp8_sdwa v73, v73 src0_sel:BYTE_3
	v_cvt_f32_fp8_sdwa v157, v74 src0_sel:BYTE_2
	v_cvt_f32_fp8_sdwa v74, v74 src0_sel:BYTE_3
	v_cvt_f32_fp8_sdwa v160, v75 src0_sel:BYTE_2
	v_cvt_f32_fp8_sdwa v75, v75 src0_sel:BYTE_3
	v_cvt_f32_fp8_sdwa v163, v76 src0_sel:BYTE_2
	v_cvt_f32_fp8_sdwa v76, v76 src0_sel:BYTE_3
	v_cvt_f32_fp8_sdwa v166, v77 src0_sel:BYTE_2
	v_cvt_f32_fp8_sdwa v77, v77 src0_sel:BYTE_3
	v_cvt_f32_fp8_sdwa v169, v78 src0_sel:BYTE_2
	v_cvt_f32_fp8_sdwa v78, v78 src0_sel:BYTE_3
	v_cvt_f32_fp8_sdwa v172, v79 src0_sel:BYTE_2
	v_cvt_f32_fp8_sdwa v79, v79 src0_sel:BYTE_3
	v_mul_f32_e32 v113, 0x3d000000, v113
	v_mul_f32_e32 v114, 0x3d000000, v114
	v_mul_f32_e32 v116, 0x3d000000, v116
	v_mul_f32_e32 v117, 0x3d000000, v117
	v_mul_f32_e32 v119, 0x3d000000, v119
	v_mul_f32_e32 v120, 0x3d000000, v120
	v_mul_f32_e32 v122, 0x3d000000, v122
	v_mul_f32_e32 v123, 0x3d000000, v123
	v_mul_f32_e32 v125, 0x3d000000, v125
	v_mul_f32_e32 v126, 0x3d000000, v126
	v_mul_f32_e32 v128, 0x3d000000, v128
	v_mul_f32_e32 v129, 0x3d000000, v129
	v_mul_f32_e32 v131, 0x3d000000, v131
	v_mul_f32_e32 v132, 0x3d000000, v132
	v_mul_f32_e32 v134, 0x3d000000, v134
	v_mul_f32_e32 v135, 0x3d000000, v135
	v_med3_f32 v6, v6, s0, v12
	v_med3_f32 v7, v7, s0, v12
	v_med3_f32 v80, v80, s0, v12
	v_med3_f32 v81, v81, s0, v12
	v_med3_f32 v83, v83, s0, v12
	v_med3_f32 v84, v84, s0, v12
	v_med3_f32 v86, v86, s0, v12
	v_med3_f32 v87, v87, s0, v12
	v_med3_f32 v89, v89, s0, v12
	v_med3_f32 v90, v90, s0, v12
	v_med3_f32 v92, v92, s0, v12
	v_med3_f32 v93, v93, s0, v12
	v_med3_f32 v95, v95, s0, v12
	v_med3_f32 v96, v96, s0, v12
	v_med3_f32 v98, v98, s0, v12
	v_med3_f32 v99, v99, s0, v12
	v_mul_f32_e32 v137, 0x3d000000, v137
	v_mul_f32_e32 v138, 0x3d000000, v138
	v_mul_f32_e32 v139, 0x3d000000, v139
	v_mul_f32_e32 v140, 0x3d000000, v140
	v_mul_f32_e32 v141, 0x3d000000, v141
	v_mul_f32_e32 v142, 0x3d000000, v142
	v_mul_f32_e32 v143, 0x3d000000, v143
	v_mul_f32_e32 v144, 0x3d000000, v144
	v_mul_f32_e32 v145, 0x3d000000, v145
	v_mul_f32_e32 v146, 0x3d000000, v146
	v_mul_f32_e32 v147, 0x3d000000, v147
	v_mul_f32_e32 v148, 0x3d000000, v148
	v_mul_f32_e32 v149, 0x3d000000, v149
	v_mul_f32_e32 v150, 0x3d000000, v150
	v_mul_f32_e32 v151, 0x3d000000, v151
	v_mul_f32_e32 v152, 0x3d000000, v152
	v_mul_f32_e32 v153, 0x3d000000, v153
	v_mul_f32_e32 v154, 0x3d000000, v154
	v_mul_f32_e32 v155, 0x3d000000, v155
	v_mul_f32_e32 v156, 0x3d000000, v156
	v_mul_f32_e32 v158, 0x3d000000, v158
	v_mul_f32_e32 v159, 0x3d000000, v159
	v_mul_f32_e32 v161, 0x3d000000, v161
	v_mul_f32_e32 v162, 0x3d000000, v162
	v_mul_f32_e32 v164, 0x3d000000, v164
	v_mul_f32_e32 v165, 0x3d000000, v165
	v_mul_f32_e32 v167, 0x3d000000, v167
	v_mul_f32_e32 v168, 0x3d000000, v168
	v_mul_f32_e32 v170, 0x3d000000, v170
	v_mul_f32_e32 v171, 0x3d000000, v171
	v_med3_f32 v101, v101, s0, v12
	v_med3_f32 v102, v102, s0, v12
	v_med3_f32 v104, v104, s0, v12
	v_med3_f32 v105, v105, s0, v12
	v_med3_f32 v107, v107, s0, v12
	v_med3_f32 v108, v108, s0, v12
	v_med3_f32 v110, v110, s0, v12
	v_med3_f32 v111, v111, s0, v12
	v_med3_f32 v113, v113, s0, v12
	v_med3_f32 v114, v114, s0, v12
	v_med3_f32 v116, v116, s0, v12
	v_med3_f32 v117, v117, s0, v12
	v_med3_f32 v119, v119, s0, v12
	v_med3_f32 v120, v120, s0, v12
	v_med3_f32 v122, v122, s0, v12
	v_med3_f32 v123, v123, s0, v12
	v_med3_f32 v125, v125, s0, v12
	v_med3_f32 v126, v126, s0, v12
	v_med3_f32 v128, v128, s0, v12
	v_med3_f32 v129, v129, s0, v12
	v_med3_f32 v131, v131, s0, v12
	v_med3_f32 v132, v132, s0, v12
	v_med3_f32 v134, v134, s0, v12
	v_med3_f32 v135, v135, s0, v12
	v_cvt_pk_fp8_f32 v19, v6, v7
	v_cvt_pk_fp8_f32 v20, v80, v81
	v_cvt_pk_fp8_f32 v21, v83, v84
	v_cvt_pk_fp8_f32 v22, v86, v87
	v_cvt_pk_fp8_f32 v23, v89, v90
	v_cvt_pk_fp8_f32 v24, v92, v93
	v_cvt_pk_fp8_f32 v25, v95, v96
	v_cvt_pk_fp8_f32 v27, v98, v99
	v_med3_f32 v6, v137, s0, v12
	v_med3_f32 v7, v138, s0, v12
	v_med3_f32 v80, v139, s0, v12
	v_med3_f32 v81, v140, s0, v12
	v_med3_f32 v83, v141, s0, v12
	v_med3_f32 v84, v142, s0, v12
	v_med3_f32 v86, v143, s0, v12
	v_med3_f32 v87, v144, s0, v12
	v_med3_f32 v89, v145, s0, v12
	v_med3_f32 v90, v146, s0, v12
	v_med3_f32 v92, v147, s0, v12
	v_med3_f32 v93, v148, s0, v12
	v_med3_f32 v95, v149, s0, v12
	v_med3_f32 v96, v150, s0, v12
	v_med3_f32 v98, v151, s0, v12
	v_med3_f32 v99, v152, s0, v12
	v_med3_f32 v137, v153, s0, v12
	v_med3_f32 v138, v154, s0, v12
	v_med3_f32 v139, v155, s0, v12
	v_med3_f32 v140, v156, s0, v12
	v_med3_f32 v142, v158, s0, v12
	v_med3_f32 v143, v159, s0, v12
	v_med3_f32 v145, v161, s0, v12
	v_med3_f32 v146, v162, s0, v12
	v_med3_f32 v148, v164, s0, v12
	v_med3_f32 v149, v165, s0, v12
	v_med3_f32 v151, v167, s0, v12
	v_med3_f32 v152, v168, s0, v12
	v_med3_f32 v154, v170, s0, v12
	v_med3_f32 v155, v171, s0, v12
	v_cvt_pk_fp8_f32 v39, v101, v102
	v_cvt_pk_fp8_f32 v40, v104, v105
	v_cvt_pk_fp8_f32 v41, v107, v108
	v_cvt_pk_fp8_f32 v42, v110, v111
	v_cvt_pk_fp8_f32 v43, v113, v114
	v_cvt_pk_fp8_f32 v44, v116, v117
	v_cvt_pk_fp8_f32 v45, v119, v120
	v_cvt_pk_fp8_f32 v46, v122, v123
	v_cvt_pk_fp8_f32 v15, v125, v126
	v_cvt_pk_fp8_f32 v16, v128, v129
	v_cvt_pk_fp8_f32 v17, v131, v132
	v_cvt_pk_fp8_f32 v18, v134, v135
	v_cvt_pk_fp8_f32 v26, v6, v7
	v_cvt_pk_fp8_f32 v28, v81, v83
	v_cvt_pk_fp8_f32 v29, v86, v87
	v_cvt_pk_fp8_f32 v30, v90, v92
	v_cvt_pk_fp8_f32 v31, v95, v96
	v_cvt_pk_fp8_f32 v32, v99, v137
	v_cvt_pk_fp8_f32 v33, v139, v140
	v_cvt_pk_fp8_f32 v34, v142, v143
	v_cvt_pk_fp8_f32 v35, v145, v146
	v_cvt_pk_fp8_f32 v36, v148, v149
	v_cvt_pk_fp8_f32 v37, v151, v152
	v_cvt_pk_fp8_f32 v38, v154, v155
	v_mul_f32_e32 v47, 0x3d000000, v47
	v_mul_f32_e32 v48, 0x3d000000, v48
	v_mul_f32_e32 v82, 0x3d000000, v82
	v_mul_f32_e32 v49, 0x3d000000, v49
	v_mul_f32_e32 v85, 0x3d000000, v85
	v_mul_f32_e32 v50, 0x3d000000, v50
	v_mul_f32_e32 v88, 0x3d000000, v88
	v_mul_f32_e32 v51, 0x3d000000, v51
	v_mul_f32_e32 v91, 0x3d000000, v91
	v_mul_f32_e32 v52, 0x3d000000, v52
	v_mul_f32_e32 v94, 0x3d000000, v94
	v_mul_f32_e32 v53, 0x3d000000, v53
	v_mul_f32_e32 v97, 0x3d000000, v97
	v_mul_f32_e32 v54, 0x3d000000, v54
	v_mul_f32_e32 v100, 0x3d000000, v100
	v_mul_f32_e32 v55, 0x3d000000, v55
	v_mul_f32_e32 v103, 0x3d000000, v103
	v_mul_f32_e32 v56, 0x3d000000, v56
	v_mul_f32_e32 v106, 0x3d000000, v106
	v_mul_f32_e32 v57, 0x3d000000, v57
	v_mul_f32_e32 v109, 0x3d000000, v109
	v_mul_f32_e32 v58, 0x3d000000, v58
	v_mul_f32_e32 v112, 0x3d000000, v112
	v_mul_f32_e32 v59, 0x3d000000, v59
	v_mul_f32_e32 v115, 0x3d000000, v115
	v_mul_f32_e32 v60, 0x3d000000, v60
	v_mul_f32_e32 v118, 0x3d000000, v118
	v_mul_f32_e32 v61, 0x3d000000, v61
	v_mul_f32_e32 v121, 0x3d000000, v121
	v_mul_f32_e32 v62, 0x3d000000, v62
	v_mul_f32_e32 v124, 0x3d000000, v124
	v_mul_f32_e32 v63, 0x3d000000, v63
	v_mul_f32_e32 v127, 0x3d000000, v127
	v_mul_f32_e32 v64, 0x3d000000, v64
	v_mul_f32_e32 v130, 0x3d000000, v130
	v_mul_f32_e32 v65, 0x3d000000, v65
	v_mul_f32_e32 v133, 0x3d000000, v133
	v_mul_f32_e32 v66, 0x3d000000, v66
	v_mul_f32_e32 v136, 0x3d000000, v136
	v_mul_f32_e32 v67, 0x3d000000, v67
	v_med3_f32 v47, v47, s0, v12
	v_med3_f32 v48, v48, s0, v12
	v_med3_f32 v82, v82, s0, v12
	v_med3_f32 v49, v49, s0, v12
	v_med3_f32 v85, v85, s0, v12
	v_med3_f32 v50, v50, s0, v12
	v_med3_f32 v88, v88, s0, v12
	v_med3_f32 v51, v51, s0, v12
	v_med3_f32 v91, v91, s0, v12
	v_med3_f32 v52, v52, s0, v12
	v_med3_f32 v94, v94, s0, v12
	v_med3_f32 v53, v53, s0, v12
	v_med3_f32 v97, v97, s0, v12
	v_med3_f32 v54, v54, s0, v12
	v_med3_f32 v100, v100, s0, v12
	v_med3_f32 v55, v55, s0, v12
	v_mul_f32_e32 v68, 0x3d000000, v68
	v_mul_f32_e32 v69, 0x3d000000, v69
	v_mul_f32_e32 v70, 0x3d000000, v70
	v_mul_f32_e32 v71, 0x3d000000, v71
	v_mul_f32_e32 v72, 0x3d000000, v72
	v_mul_f32_e32 v73, 0x3d000000, v73
	v_mul_f32_e32 v157, 0x3d000000, v157
	v_mul_f32_e32 v74, 0x3d000000, v74
	v_mul_f32_e32 v160, 0x3d000000, v160
	v_mul_f32_e32 v75, 0x3d000000, v75
	v_mul_f32_e32 v163, 0x3d000000, v163
	v_mul_f32_e32 v76, 0x3d000000, v76
	v_mul_f32_e32 v166, 0x3d000000, v166
	v_mul_f32_e32 v77, 0x3d000000, v77
	v_mul_f32_e32 v169, 0x3d000000, v169
	v_mul_f32_e32 v78, 0x3d000000, v78
	v_mul_f32_e32 v172, 0x3d000000, v172
	v_mul_f32_e32 v79, 0x3d000000, v79
	v_med3_f32 v103, v103, s0, v12
	v_med3_f32 v56, v56, s0, v12
	v_med3_f32 v106, v106, s0, v12
	v_med3_f32 v57, v57, s0, v12
	v_med3_f32 v109, v109, s0, v12
	v_med3_f32 v58, v58, s0, v12
	v_med3_f32 v112, v112, s0, v12
	v_med3_f32 v59, v59, s0, v12
	v_med3_f32 v115, v115, s0, v12
	v_med3_f32 v60, v60, s0, v12
	v_med3_f32 v118, v118, s0, v12
	v_med3_f32 v61, v61, s0, v12
	v_med3_f32 v121, v121, s0, v12
	v_med3_f32 v62, v62, s0, v12
	v_med3_f32 v124, v124, s0, v12
	v_med3_f32 v63, v63, s0, v12
	v_med3_f32 v127, v127, s0, v12
	v_med3_f32 v64, v64, s0, v12
	v_med3_f32 v130, v130, s0, v12
	v_med3_f32 v65, v65, s0, v12
	v_med3_f32 v133, v133, s0, v12
	v_med3_f32 v66, v66, s0, v12
	v_med3_f32 v136, v136, s0, v12
	v_med3_f32 v67, v67, s0, v12
	v_med3_f32 v68, v68, s0, v12
	v_med3_f32 v69, v69, s0, v12
	v_med3_f32 v70, v70, s0, v12
	v_med3_f32 v71, v71, s0, v12
	v_med3_f32 v72, v72, s0, v12
	v_med3_f32 v73, v73, s0, v12
	v_med3_f32 v141, v157, s0, v12
	v_med3_f32 v74, v74, s0, v12
	v_med3_f32 v144, v160, s0, v12
	v_med3_f32 v75, v75, s0, v12
	v_med3_f32 v147, v163, s0, v12
	v_med3_f32 v76, v76, s0, v12
	v_med3_f32 v150, v166, s0, v12
	v_med3_f32 v77, v77, s0, v12
	v_med3_f32 v153, v169, s0, v12
	v_med3_f32 v78, v78, s0, v12
	v_med3_f32 v156, v172, s0, v12
	v_med3_f32 v79, v79, s0, v12
	v_cvt_pk_fp8_f32 v19, v47, v48 op_sel:[0,0,1]
	v_cvt_pk_fp8_f32 v20, v82, v49 op_sel:[0,0,1]
	v_cvt_pk_fp8_f32 v21, v85, v50 op_sel:[0,0,1]
	v_cvt_pk_fp8_f32 v22, v88, v51 op_sel:[0,0,1]
	v_cvt_pk_fp8_f32 v23, v91, v52 op_sel:[0,0,1]
	v_cvt_pk_fp8_f32 v24, v94, v53 op_sel:[0,0,1]
	v_cvt_pk_fp8_f32 v25, v97, v54 op_sel:[0,0,1]
	v_cvt_pk_fp8_f32 v27, v100, v55 op_sel:[0,0,1]
	v_cvt_pk_fp8_f32 v39, v103, v56 op_sel:[0,0,1]
	v_cvt_pk_fp8_f32 v40, v106, v57 op_sel:[0,0,1]
	v_cvt_pk_fp8_f32 v41, v109, v58 op_sel:[0,0,1]
	v_cvt_pk_fp8_f32 v42, v112, v59 op_sel:[0,0,1]
	v_cvt_pk_fp8_f32 v43, v115, v60 op_sel:[0,0,1]
	v_cvt_pk_fp8_f32 v44, v118, v61 op_sel:[0,0,1]
	v_cvt_pk_fp8_f32 v45, v121, v62 op_sel:[0,0,1]
	v_cvt_pk_fp8_f32 v46, v124, v63 op_sel:[0,0,1]
	v_cvt_pk_fp8_f32 v15, v127, v64 op_sel:[0,0,1]
	v_cvt_pk_fp8_f32 v16, v130, v65 op_sel:[0,0,1]
	v_cvt_pk_fp8_f32 v17, v133, v66 op_sel:[0,0,1]
	v_cvt_pk_fp8_f32 v18, v136, v67 op_sel:[0,0,1]
	v_cvt_pk_fp8_f32 v26, v80, v68 op_sel:[0,0,1]
	v_cvt_pk_fp8_f32 v28, v84, v69 op_sel:[0,0,1]
	v_cvt_pk_fp8_f32 v29, v89, v70 op_sel:[0,0,1]
	v_cvt_pk_fp8_f32 v30, v93, v71 op_sel:[0,0,1]
	v_cvt_pk_fp8_f32 v31, v98, v72 op_sel:[0,0,1]
	v_cvt_pk_fp8_f32 v32, v138, v73 op_sel:[0,0,1]
	v_cvt_pk_fp8_f32 v33, v141, v74 op_sel:[0,0,1]
	v_cvt_pk_fp8_f32 v34, v144, v75 op_sel:[0,0,1]
	v_cvt_pk_fp8_f32 v35, v147, v76 op_sel:[0,0,1]
	v_cvt_pk_fp8_f32 v36, v150, v77 op_sel:[0,0,1]
	v_cvt_pk_fp8_f32 v37, v153, v78 op_sel:[0,0,1]
	v_cvt_pk_fp8_f32 v38, v156, v79 op_sel:[0,0,1]
	v_and_b32_e32 v6, 0x1f1f1f1f, v19
	v_lshrrev_b32_e32 v7, 2, v19
	v_and_b32_e32 v19, 0x1f1f1f1f, v20
	v_lshrrev_b32_e32 v20, 2, v20
	v_and_b32_e32 v47, 0x1f1f1f1f, v21
	v_lshrrev_b32_e32 v21, 2, v21
	v_and_b32_e32 v48, 0x1f1f1f1f, v22
	v_lshrrev_b32_e32 v22, 2, v22
	v_and_b32_e32 v49, 0x1f1f1f1f, v23
	v_lshrrev_b32_e32 v23, 2, v23
	v_and_b32_e32 v50, 0x1f1f1f1f, v24
	v_lshrrev_b32_e32 v24, 2, v24
	v_and_b32_e32 v51, 0x1f1f1f1f, v25
	v_lshrrev_b32_e32 v25, 2, v25
	v_and_b32_e32 v52, 0x1f1f1f1f, v27
	v_lshrrev_b32_e32 v27, 2, v27
	v_and_b32_e32 v53, 0x1f1f1f1f, v39
	v_lshrrev_b32_e32 v39, 2, v39
	v_and_b32_e32 v54, 0x1f1f1f1f, v40
	v_lshrrev_b32_e32 v40, 2, v40
	v_and_b32_e32 v55, 0x1f1f1f1f, v41
	v_lshrrev_b32_e32 v41, 2, v41
	v_and_b32_e32 v56, 0x1f1f1f1f, v42
	v_lshrrev_b32_e32 v42, 2, v42
	v_and_b32_e32 v57, 0x1f1f1f1f, v43
	v_lshrrev_b32_e32 v43, 2, v43
	v_and_b32_e32 v58, 0x1f1f1f1f, v44
	v_lshrrev_b32_e32 v44, 2, v44
	v_and_b32_e32 v59, 0x1f1f1f1f, v45
	v_lshrrev_b32_e32 v45, 2, v45
	v_and_b32_e32 v60, 0x1f1f1f1f, v46
	v_lshrrev_b32_e32 v46, 2, v46
	v_and_b32_e32 v61, 0x1f1f1f1f, v15
	v_lshrrev_b32_e32 v15, 2, v15
	v_and_b32_e32 v62, 0x1f1f1f1f, v16
	v_lshrrev_b32_e32 v63, 2, v16
	v_and_b32_e32 v64, 0x1f1f1f1f, v17
	v_lshrrev_b32_e32 v65, 2, v17
	v_and_b32_e32 v66, 0x1f1f1f1f, v18
	v_lshrrev_b32_e32 v67, 2, v18
	v_and_or_b32 v16, v7, s1, v6
	v_and_or_b32 v17, v20, s1, v19
	v_and_or_b32 v18, v21, s1, v47
	v_and_or_b32 v19, v22, s1, v48
	v_and_or_b32 v20, v23, s1, v49
	v_and_or_b32 v21, v24, s1, v50
	v_and_or_b32 v22, v25, s1, v51
	v_and_or_b32 v23, v27, s1, v52
	v_and_b32_e32 v6, 0x1f1f1f1f, v26
	v_lshrrev_b32_e32 v7, 2, v26
	v_and_b32_e32 v47, 0x1f1f1f1f, v28
	v_lshrrev_b32_e32 v48, 2, v28
	v_and_b32_e32 v49, 0x1f1f1f1f, v29
	v_lshrrev_b32_e32 v50, 2, v29
	v_and_b32_e32 v51, 0x1f1f1f1f, v30
	v_lshrrev_b32_e32 v52, 2, v30
	v_and_b32_e32 v68, 0x1f1f1f1f, v31
	v_lshrrev_b32_e32 v69, 2, v31
	v_and_b32_e32 v70, 0x1f1f1f1f, v32
	v_lshrrev_b32_e32 v71, 2, v32
	v_and_b32_e32 v72, 0x1f1f1f1f, v33
	v_lshrrev_b32_e32 v73, 2, v33
	v_and_b32_e32 v74, 0x1f1f1f1f, v34
	v_lshrrev_b32_e32 v75, 2, v34
	v_and_b32_e32 v76, 0x1f1f1f1f, v35
	v_lshrrev_b32_e32 v77, 2, v35
	v_and_b32_e32 v78, 0x1f1f1f1f, v36
	v_lshrrev_b32_e32 v79, 2, v36
	v_and_b32_e32 v80, 0x1f1f1f1f, v37
	v_lshrrev_b32_e32 v81, 2, v37
	v_and_b32_e32 v82, 0x1f1f1f1f, v38
	v_lshrrev_b32_e32 v83, 2, v38
	v_and_or_b32 v24, v39, s1, v53
	v_and_or_b32 v25, v40, s1, v54
	v_and_or_b32 v26, v41, s1, v55
	v_and_or_b32 v27, v42, s1, v56
	v_and_or_b32 v28, v43, s1, v57
	v_and_or_b32 v29, v44, s1, v58
	v_and_or_b32 v30, v45, s1, v59
	v_and_or_b32 v31, v46, s1, v60
	v_and_or_b32 v32, v15, s1, v61
	v_and_or_b32 v33, v63, s1, v62
	v_and_or_b32 v34, v65, s1, v64
	v_and_or_b32 v35, v67, s1, v66
	ds_write_b128 v14, v[16:19] offset:16
	ds_write_b128 v14, v[20:23] offset:32
	v_and_or_b32 v16, v7, s1, v6
	v_and_or_b32 v17, v48, s1, v47
	v_and_or_b32 v18, v50, s1, v49
	v_and_or_b32 v19, v52, s1, v51
	v_and_or_b32 v20, v69, s1, v68
	v_and_or_b32 v21, v71, s1, v70
	v_and_or_b32 v22, v73, s1, v72
	v_and_or_b32 v23, v75, s1, v74
	v_and_or_b32 v36, v77, s1, v76
	v_and_or_b32 v37, v79, s1, v78
	v_and_or_b32 v38, v81, s1, v80
	v_and_or_b32 v39, v83, s1, v82
	ds_write_b128 v14, v[24:27] offset:96
	ds_write_b128 v14, v[28:31] offset:112
	ds_write_b128 v14, v[32:35]
	ds_write_b128 v14, v[16:19] offset:48
	ds_write_b128 v14, v[20:23] offset:64
	ds_write_b128 v14, v[36:39] offset:80
	s_waitcnt lgkmcnt(0)
	ds_read_u8 v6, v13
	ds_read_u8 v7, v13 offset:144
	ds_read_u8 v15, v13 offset:288
	ds_read_u8 v16, v13 offset:432
	ds_read_u8 v17, v13 offset:496
	ds_read_u8 v18, v13 offset:352
	ds_read_u8 v19, v13 offset:208
	ds_read_u8 v20, v13 offset:64
	ds_read_u8 v21, v13 offset:1152
	ds_read_u8 v22, v13 offset:1296
	ds_read_u8 v23, v13 offset:1440
	ds_read_u8 v24, v13 offset:1584
	ds_read_u8 v25, v13 offset:1648
	ds_read_u8 v26, v13 offset:1504
	ds_read_u8 v27, v13 offset:1360
	ds_read_u8 v28, v13 offset:1216
	ds_read_u8 v29, v13 offset:2304
	ds_read_u8 v30, v13 offset:2448
	ds_read_u8 v31, v13 offset:2592
	ds_read_u8 v32, v13 offset:2736
	ds_read_u8 v33, v13 offset:2800
	ds_read_u8 v34, v13 offset:2656
	ds_read_u8 v35, v13 offset:2512
	ds_read_u8 v36, v13 offset:2368
	ds_read_u8 v37, v13 offset:3456
	ds_read_u8 v38, v13 offset:3600
	ds_read_u8 v39, v13 offset:3744
	ds_read_u8 v40, v13 offset:3888
	ds_read_u8 v41, v13 offset:3952
	ds_read_u8 v42, v13 offset:3808
	ds_read_u8 v43, v13 offset:3664
	ds_read_u8 v44, v13 offset:3520
	ds_read_u8 v45, v13 offset:4608
	ds_read_u8 v46, v13 offset:4752
	ds_read_u8 v47, v13 offset:4896
	ds_read_u8 v48, v13 offset:5040
	ds_read_u8 v49, v13 offset:5104
	ds_read_u8 v50, v13 offset:4960
	ds_read_u8 v51, v13 offset:4816
	ds_read_u8 v52, v13 offset:4672
	ds_read_u8 v53, v13 offset:5760
	ds_read_u8 v54, v13 offset:5904
	ds_read_u8 v55, v13 offset:6048
	ds_read_u8 v56, v13 offset:6192
	ds_read_u8 v57, v13 offset:6256
	ds_read_u8 v58, v13 offset:6112
	ds_read_u8 v59, v13 offset:5968
	ds_read_u8 v60, v13 offset:5824
	ds_read_u8 v61, v13 offset:6912
	ds_read_u8 v62, v13 offset:7056
	ds_read_u8 v63, v13 offset:7200
	ds_read_u8 v64, v13 offset:7344
	ds_read_u8 v65, v13 offset:7408
	ds_read_u8 v66, v13 offset:7264
	ds_read_u8 v67, v13 offset:7120
	ds_read_u8 v68, v13 offset:6976
	ds_read_u8 v69, v13 offset:8064
	ds_read_u8 v70, v13 offset:8208
	ds_read_u8 v71, v13 offset:8352
	ds_read_u8 v72, v13 offset:8496
	ds_read_u8 v73, v13 offset:8560
	ds_read_u8 v74, v13 offset:8416
	ds_read_u8 v75, v13 offset:8272
	ds_read_u8 v76, v13 offset:8128
	ds_read_u8 v77, v13 offset:576
	ds_read_u8 v78, v13 offset:720
	ds_read_u8 v79, v13 offset:864
	ds_read_u8 v80, v13 offset:1008
	ds_read_u8 v81, v13 offset:1072
	ds_read_u8 v82, v13 offset:928
	ds_read_u8 v83, v13 offset:784
	ds_read_u8 v84, v13 offset:640
	ds_read_u8 v85, v13 offset:1728
	ds_read_u8 v86, v13 offset:1872
	ds_read_u8 v87, v13 offset:2016
	ds_read_u8 v88, v13 offset:2160
	ds_read_u8 v89, v13 offset:2224
	ds_read_u8 v90, v13 offset:2080
	ds_read_u8 v91, v13 offset:1936
	ds_read_u8 v92, v13 offset:1792
	ds_read_u8 v93, v13 offset:2880
	ds_read_u8 v94, v13 offset:3024
	ds_read_u8 v95, v13 offset:3168
	ds_read_u8 v96, v13 offset:3312
	ds_read_u8 v97, v13 offset:3376
	ds_read_u8 v98, v13 offset:3232
	ds_read_u8 v99, v13 offset:3088
	ds_read_u8 v100, v13 offset:2944
	ds_read_u8 v101, v13 offset:4032
	ds_read_u8 v102, v13 offset:4176
	ds_read_u8 v103, v13 offset:4320
	ds_read_u8 v104, v13 offset:4464
	ds_read_u8 v105, v13 offset:4528
	ds_read_u8 v106, v13 offset:4384
	ds_read_u8 v107, v13 offset:4240
	ds_read_u8 v108, v13 offset:4096
	ds_read_u8 v109, v13 offset:5184
	ds_read_u8 v110, v13 offset:5328
	ds_read_u8 v111, v13 offset:5472
	ds_read_u8 v112, v13 offset:5616
	ds_read_u8 v113, v13 offset:5680
	ds_read_u8 v114, v13 offset:5536
	ds_read_u8 v115, v13 offset:5392
	ds_read_u8 v116, v13 offset:5248
	ds_read_u8 v117, v13 offset:6336
	ds_read_u8 v118, v13 offset:6480
	ds_read_u8 v119, v13 offset:6624
	ds_read_u8 v120, v13 offset:6768
	ds_read_u8 v121, v13 offset:6832
	ds_read_u8 v122, v13 offset:6688
	ds_read_u8 v123, v13 offset:6544
	ds_read_u8 v124, v13 offset:6400
	ds_read_u8 v125, v13 offset:7488
	ds_read_u8 v126, v13 offset:7632
	ds_read_u8 v127, v13 offset:7776
	ds_read_u8 v128, v13 offset:7920
	ds_read_u8 v129, v13 offset:7984
	ds_read_u8 v130, v13 offset:7840
	ds_read_u8 v131, v13 offset:7696
	ds_read_u8 v132, v13 offset:7552
	ds_read_u8 v133, v13 offset:8640
	ds_read_u8 v134, v13 offset:8784
	ds_read_u8 v135, v13 offset:8928
	ds_read_u8 v136, v13 offset:9072
	ds_read_u8 v137, v13 offset:9136
	ds_read_u8 v138, v13 offset:8992
	ds_read_u8 v139, v13 offset:8848
	ds_read_u8 v140, v13 offset:8704
	s_waitcnt lgkmcnt(14)
	v_lshl_or_b32 v6, v7, 12, v6
	v_lshlrev_b32_e32 v7, 24, v15
	v_lshlrev_b32_e32 v15, 4, v16
	v_lshrrev_b32_e32 v16, 4, v22
	v_lshlrev_b32_e32 v141, 28, v22
	v_lshl_or_b32 v22, v30, 12, v29
	v_lshlrev_b32_e32 v29, 24, v31
	v_lshlrev_b32_e32 v30, 4, v32
	v_lshlrev_b32_e32 v31, 28, v38
	v_lshrrev_b32_e32 v32, 4, v38
	v_lshlrev_b32_e32 v38, 6, v45
	v_lshlrev_b32_e32 v61, 6, v61
	v_lshl_or_b32 v77, v78, 12, v77
	v_lshlrev_b32_e32 v78, 24, v79
	v_lshlrev_b32_e32 v79, 4, v80
	v_lshlrev_b32_e32 v80, 28, v86
	v_lshrrev_b32_e32 v86, 4, v86
	v_lshl_or_b32 v93, v94, 12, v93
	v_lshlrev_b32_e32 v94, 24, v95
	v_lshlrev_b32_e32 v95, 4, v96
	v_lshlrev_b32_e32 v96, 28, v102
	v_lshrrev_b32_e32 v102, 4, v102
	v_lshlrev_b32_e32 v109, 6, v109
	v_lshlrev_b32_e32 v125, 6, v125
	v_lshl_or_b32 v19, v19, 12, v20
	v_lshlrev_b32_e32 v18, 24, v18
	v_lshlrev_b32_e32 v17, 4, v17
	v_lshlrev_b32_e32 v145, 28, v27
	v_lshrrev_b32_e32 v20, 4, v27
	v_lshl_or_b32 v27, v35, 12, v36
	v_lshlrev_b32_e32 v33, 4, v33
	v_lshlrev_b32_e32 v35, 28, v43
	v_lshrrev_b32_e32 v36, 4, v43
	v_lshlrev_b32_e32 v43, 6, v52
	v_lshl_or_b32 v83, v83, 12, v84
	v_lshlrev_b32_e32 v84, 28, v91
	v_lshrrev_b32_e32 v91, 4, v91
	v_lshl_or_b32 v99, v99, 12, v100
	v_lshlrev_b32_e32 v97, 4, v97
	v_lshlrev_b32_e32 v100, 28, v107
	v_lshrrev_b32_e32 v107, 4, v107
	v_lshl_or_b32 v16, v23, 8, v16
	v_lshlrev_b32_e32 v45, 18, v46
	v_lshlrev_b32_e32 v46, 30, v47
	v_lshrrev_b32_e32 v47, 2, v47
	v_lshlrev_b32_e32 v62, 18, v62
	v_lshlrev_b32_e32 v142, 30, v63
	v_lshrrev_b32_e32 v63, 2, v63
	v_lshlrev_b32_e32 v110, 18, v110
	v_lshlrev_b32_e32 v143, 30, v111
	v_lshrrev_b32_e32 v111, 2, v111
	v_lshlrev_b32_e32 v126, 18, v126
	s_waitcnt lgkmcnt(13)
	v_lshlrev_b32_e32 v144, 30, v127
	v_lshrrev_b32_e32 v127, 2, v127
	v_lshlrev_b32_e32 v34, 24, v34
	v_lshlrev_b32_e32 v51, 18, v51
	v_lshlrev_b32_e32 v52, 30, v50
	v_lshrrev_b32_e32 v50, 2, v50
	v_lshlrev_b32_e32 v68, 6, v68
	v_lshlrev_b32_e32 v146, 30, v66
	v_lshrrev_b32_e32 v66, 2, v66
	v_lshlrev_b32_e32 v81, 4, v81
	s_waitcnt lgkmcnt(10)
	v_lshlrev_b32_e32 v148, 30, v130
	v_lshrrev_b32_e32 v130, 2, v130
	v_lshl_or_b32 v15, v21, 16, v15
	v_lshl_or_b32 v21, v37, 16, v30
	v_lshl_or_b32 v23, v39, 8, v32
	v_or3_b32 v6, v6, v7, v38
	v_or3_b32 v7, v22, v29, v61
	v_lshl_or_b32 v22, v85, 16, v79
	v_lshl_or_b32 v29, v87, 8, v86
	v_lshl_or_b32 v30, v101, 16, v95
	v_lshl_or_b32 v32, v103, 8, v102
	v_or3_b32 v37, v77, v78, v109
	v_or3_b32 v38, v93, v94, v125
	v_lshl_or_b32 v17, v28, 16, v17
	v_lshl_or_b32 v26, v26, 8, v20
	v_lshl_or_b32 v28, v44, 16, v33
	v_lshl_or_b32 v33, v42, 8, v36
	v_or3_b32 v18, v19, v18, v43
	v_lshl_or_b32 v36, v90, 8, v91
	v_lshl_or_b32 v39, v108, 16, v97
	v_lshl_or_b32 v42, v106, 8, v107
	v_lshl_or_b32 v61, v24, 20, v16
	v_lshlrev_b32_e32 v48, 10, v48
	v_lshlrev_b32_e32 v53, 22, v53
	v_lshlrev_b32_e32 v55, 14, v55
	v_lshlrev_b32_e32 v56, 26, v56
	v_lshlrev_b32_e32 v64, 10, v64
	v_lshlrev_b32_e32 v69, 22, v69
	v_lshlrev_b32_e32 v49, 10, v49
	v_lshlrev_b32_e32 v60, 22, v60
	v_lshlrev_b32_e32 v82, 24, v82
	v_lshlrev_b32_e32 v98, 24, v98
	v_lshlrev_b32_e32 v116, 6, v116
	v_lshlrev_b32_e32 v147, 30, v114
	v_lshrrev_b32_e32 v114, 2, v114
	s_waitcnt lgkmcnt(8)
	v_lshlrev_b32_e32 v132, 6, v132
	v_or3_b32 v27, v27, v34, v68
	v_lshl_or_b32 v34, v92, 16, v81
	v_lshl_or_b32 v40, v40, 20, v23
	v_or3_b32 v16, v6, v45, v46
	v_or3_b32 v6, v15, v141, v47
	v_or3_b32 v19, v7, v62, v142
	v_or3_b32 v7, v21, v31, v63
	v_lshl_or_b32 v15, v88, 20, v29
	v_lshl_or_b32 v29, v104, 20, v32
	v_or3_b32 v20, v37, v110, v143
	v_or3_b32 v21, v22, v80, v111
	v_or3_b32 v23, v38, v126, v144
	v_or3_b32 v22, v30, v96, v127
	v_lshl_or_b32 v26, v25, 20, v26
	v_lshl_or_b32 v30, v41, 20, v33
	v_or3_b32 v24, v18, v51, v52
	v_or3_b32 v18, v17, v145, v50
	v_or3_b32 v33, v28, v35, v66
	v_lshl_or_b32 v35, v89, 20, v36
	v_lshl_or_b32 v37, v105, 20, v42
	v_or3_b32 v38, v39, v100, v130
	v_lshl_or_b32 v39, v54, 2, v61
	v_lshlrev_b32_e32 v71, 14, v71
	v_lshlrev_b32_e32 v72, 26, v72
	v_lshlrev_b32_e32 v112, 10, v112
	v_lshlrev_b32_e32 v117, 22, v117
	v_lshlrev_b32_e32 v119, 14, v119
	v_lshlrev_b32_e32 v120, 26, v120
	v_lshlrev_b32_e32 v128, 10, v128
	s_waitcnt lgkmcnt(7)
	v_lshlrev_b32_e32 v133, 22, v133
	s_waitcnt lgkmcnt(5)
	v_lshlrev_b32_e32 v135, 14, v135
	s_waitcnt lgkmcnt(4)
	v_lshlrev_b32_e32 v136, 26, v136
	v_lshlrev_b32_e32 v58, 14, v58
	v_lshlrev_b32_e32 v57, 26, v57
	v_lshlrev_b32_e32 v67, 18, v67
	v_lshlrev_b32_e32 v65, 10, v65
	v_lshlrev_b32_e32 v76, 22, v76
	v_lshlrev_b32_e32 v74, 14, v74
	v_lshlrev_b32_e32 v73, 26, v73
	v_lshlrev_b32_e32 v115, 18, v115
	v_lshlrev_b32_e32 v113, 10, v113
	v_lshlrev_b32_e32 v124, 22, v124
	v_lshlrev_b32_e32 v122, 14, v122
	v_lshlrev_b32_e32 v121, 26, v121
	v_lshlrev_b32_e32 v131, 18, v131
	v_lshlrev_b32_e32 v129, 10, v129
	s_waitcnt lgkmcnt(0)
	v_lshlrev_b32_e32 v140, 22, v140
	v_lshlrev_b32_e32 v138, 14, v138
	v_lshlrev_b32_e32 v137, 26, v137
	v_or3_b32 v43, v83, v82, v116
	v_or3_b32 v44, v99, v98, v132
	v_or3_b32 v36, v34, v84, v114
	v_or3_b32 v17, v6, v48, v53
	v_or3_b32 v6, v7, v64, v69
	v_lshl_or_b32 v7, v70, 2, v40
	v_lshl_or_b32 v15, v118, 2, v15
	v_lshl_or_b32 v40, v134, 2, v29
	v_or3_b32 v25, v18, v49, v60
	v_lshl_or_b32 v26, v59, 2, v26
	v_lshl_or_b32 v30, v75, 2, v30
	v_lshl_or_b32 v41, v123, 2, v35
	v_lshl_or_b32 v37, v139, 2, v37
	v_or3_b32 v18, v39, v55, v56
	v_or3_b32 v27, v27, v67, v146
	v_or3_b32 v28, v43, v115, v147
	v_or3_b32 v31, v44, v131, v148
	v_or3_b32 v21, v21, v112, v117
	v_or3_b32 v32, v22, v128, v133
	v_or3_b32 v34, v33, v65, v76
	v_or3_b32 v29, v36, v113, v124
	v_or3_b32 v36, v38, v129, v140
	v_or3_b32 v7, v7, v71, v72
	v_or3_b32 v22, v15, v119, v120
	v_or3_b32 v33, v40, v135, v136
	v_or3_b32 v26, v26, v58, v57
	v_or3_b32 v35, v30, v74, v73
	v_or3_b32 v30, v41, v122, v121
	v_or3_b32 v37, v37, v138, v137
	v_mbcnt_lo_u32_b32 v202, -1, 0
	v_mbcnt_hi_u32_b32 v202, -1, v202
	v_and_b32_e32 v202, 16, v202
	v_lshrrev_b32_e32 v202, 1, v202
	v_mov_b32_e32 v203, 0
	v_lshl_add_u64 v[200:201], v[10:11], 0, v[202:203]
	v_lshl_add_u64 v[204:205], v[8:9], 0, v[202:203]
	global_store_dwordx4 v[10:11], v[16:19], off
	global_store_dwordx2 v[200:201], v[6:7], off offset:16
	global_store_dwordx4 v[10:11], v[20:23], off offset:32
	global_store_dwordx2 v[200:201], v[32:33], off offset:48
	global_store_dwordx4 v[8:9], v[24:27], off
	global_store_dwordx2 v[204:205], v[34:35], off offset:16
	global_store_dwordx4 v[8:9], v[28:31], off offset:32
	global_store_dwordx2 v[204:205], v[36:37], off offset:48
	s_waitcnt lgkmcnt(0)
	s_cbranch_scc1 .LBB0_316

.LBB0_413:
	v_bfe_u32 v3, v9, 1, 3
	v_ashrrev_i32_e32 v7, 4, v9
	v_lshlrev_b32_e32 v6, 7, v8
	v_and_b32_e32 v10, -2, v7
	v_bitop3_b32 v11, v7, v3, -2 bitop3:0x6c
	v_bitop3_b32 v3, v7, v3, 1 bitop3:0x36
	v_lshrrev_b32_e32 v2, 1, v9
	v_lshl_add_u32 v224, v3, 4, v6
	v_add_u32_e32 v3, 4, v10
	v_bitop3_b32 v3, v3, v2, 7 bitop3:0x78
	v_lshl_add_u32 v221, v3, 4, v6
	v_add_u32_e32 v3, 5, v10
	v_bitop3_b32 v2, v3, v2, 7 bitop3:0x78
	v_lshl_add_u32 v222, v2, 4, v6
	v_bfe_u32 v2, v9, 2, 2
	v_lshl_add_u32 v223, v11, 4, v6
	v_lshlrev_b32_e32 v3, 6, v8
	v_bitop3_b32 v6, v7, v2, -2 bitop3:0x6c
	v_bitop3_b32 v2, v7, v2, 1 bitop3:0x36
	v_lshl_add_u32 v220, v2, 4, v3
	v_and_b32_e32 v10, 16, v9
	v_lshrrev_b32_e32 v10, 1, v10
	v_add_u32_e32 v224, v224, v10
	v_add_u32_e32 v222, v222, v10
	v_add_u32_e32 v220, v220, v10
	s_waitcnt vmcnt(0)
	s_barrier
	v_add_u32_e32 v2, 0, v223
	v_lshl_add_u32 v163, v6, 4, v3
	v_add_u32_e32 v3, 0, v224
	ds_read_b128 v[6:9], v2
	ds_read_b64 v[10:11], v3
	v_mov_b32_e32 v186, v4
	v_mov_b32_e32 v187, v5
	ds_read_b128 v[12:15], v2 offset:4096
	ds_read_b64 v[16:17], v3 offset:4096
	s_waitcnt lgkmcnt(0)
	v_mfma_scale_f32_32x32x64_f8f6f4 v[32:47], v[6:11], v[182:187], 0, v217, v216 op_sel_hi:[0,0,0] cbsz:2 blgp:2
	v_mov_b32_e32 v180, v0
	v_add_u32_e32 v2, 0, v221
	v_add_u32_e32 v3, 0, v222
	ds_read_b128 v[52:55], v2
	ds_read_b64 v[56:57], v3
	v_mov_b32_e32 v181, v1
	ds_read_b128 v[58:61], v2 offset:4096
	ds_read_b64 v[62:63], v3 offset:4096
	s_waitcnt vmcnt(0) lgkmcnt(0)
	v_mfma_scale_f32_32x32x64_f8f6f4 v[32:47], v[52:57], v[176:181], v[32:47], v217, v216 op_sel_hi:[0,0,0] cbsz:2 blgp:2
	s_barrier
	s_mov_b32 m0, s89
	s_cmp_lg_u64 s[60:61], 0
	global_load_lds_dwordx4 v[228:229], off
	s_cbranch_scc1 .Lpro_noconv
	v_mbcnt_lo_u32_b32 v98, -1, 0
	v_mbcnt_hi_u32_b32 v98, -1, v98
	s_mov_b32 m0, s87
	v_ashrrev_i32_e32 v96, 3, v98
	v_mad_i64_i32 v[96:97], s[10:11], s56, v96, 0
	v_lshlrev_b32_e32 v98, 4, v98
	v_lshl_add_u64 v[96:97], v[96:97], 2, s[58:59]
	v_and_b32_e32 v166, 0x70, v98
	v_lshl_add_u64 v[96:97], v[96:97], 0, v[166:167]
	global_load_lds_dwordx4 v[96:97], off nt
